# deleted 40 duplicate s_waitcnt lgkmcnt(0) (compiler copy right after the asm one, only s_setprio between) in the GEMM K-loops (on top of v60)
# speedup vs baseline: 1.0111x; 1.0029x over previous
.Lpeel_in:
	s_mov_b64 s[26:27], 0
	v_mov_b64_e32 v[178:179], v[174:175]
	v_mov_b64_e32 v[180:181], v[168:169]
	v_mov_b32_e32 v186, v176
	v_mov_b32_e32 v172, v170
	ds_read_b128 v[0:3], v193
	ds_read_b128 v[8:11], v193 offset:2048
	ds_read_b128 v[4:7], v195
	ds_read_b128 v[12:15], v195 offset:2048
	s_add_u32 s15, s24, 0x80
	s_addc_u32 s23, s25, 0
	s_and_b64 s[26:27], s[26:27], exec
	s_cselect_b32 s29, s19, s23
	s_cselect_b32 s28, s18, s15
	s_cselect_b32 s27, s17, s3
	s_cselect_b32 s26, s16, s2
	v_lshl_add_u64 v[16:17], s[24:25], 0, v[168:169]
	s_add_i32 m0, s47, 0xc000
	ds_read_b128 v[218:221], v192
	ds_read_b128 v[226:229], v192 offset:2048
	ds_read_b128 v[222:225], v194
	ds_read_b128 v[230:233], v194 offset:2048
	ds_read_b128 v[234:237], v192 offset:4096
	ds_read_b128 v[242:245], v192 offset:6144
	ds_read_b128 v[238:241], v194 offset:4096
	ds_read_b128 v[246:249], v194 offset:6144
	global_load_lds_dwordx4 v[16:17], off
	v_lshl_add_u64 v[16:17], s[24:25], 0, v[174:175]
	s_add_i32 m0, s47, 0xe000
	s_nop 0
	global_load_lds_dwordx4 v[16:17], off
	s_waitcnt lgkmcnt(8)
	s_barrier
	s_waitcnt lgkmcnt(0)
	s_setprio 1
	v_mfma_scale_f32_16x16x128_f8f6f4 v[156:159], v[0:7], v[218:225], 0, v191, v191 op_sel_hi:[0,0,0]
	v_mfma_scale_f32_16x16x128_f8f6f4 v[152:155], v[8:15], v[218:225], 0, v191, v191 op_sel_hi:[0,0,0]
	v_mfma_scale_f32_16x16x128_f8f6f4 v[148:151], v[0:7], v[226:233], 0, v191, v191 op_sel_hi:[0,0,0]
	v_mfma_scale_f32_16x16x128_f8f6f4 v[144:147], v[8:15], v[226:233], 0, v191, v191 op_sel_hi:[0,0,0]
	v_mfma_scale_f32_16x16x128_f8f6f4 v[140:143], v[0:7], v[234:241], 0, v191, v191 op_sel_hi:[0,0,0]
	v_mfma_scale_f32_16x16x128_f8f6f4 v[136:139], v[8:15], v[234:241], 0, v191, v191 op_sel_hi:[0,0,0]
	v_mfma_scale_f32_16x16x128_f8f6f4 v[132:135], v[0:7], v[242:249], 0, v191, v191 op_sel_hi:[0,0,0]
	v_mfma_scale_f32_16x16x128_f8f6f4 v[128:131], v[8:15], v[242:249], 0, v191, v191 op_sel_hi:[0,0,0]
	s_setprio 0
	s_barrier
	s_mov_b32 m0, s30
	v_lshl_add_u64 v[182:183], s[26:27], 0, v[162:163]
	ds_read_b128 v[16:19], v193 offset:16384
	ds_read_b128 v[24:27], v193 offset:18432
	ds_read_b128 v[20:23], v195 offset:16384
	ds_read_b128 v[28:31], v195 offset:18432
	global_load_lds_dwordx4 v[182:183], off
	v_lshl_add_u64 v[184:185], s[26:27], 0, v[164:165]
	s_mov_b32 m0, s46
	s_nop 0
	global_load_lds_dwordx4 v[184:185], off
	s_barrier
	s_waitcnt lgkmcnt(0)
	s_setprio 1
	v_mfma_scale_f32_16x16x128_f8f6f4 v[92:95], v[16:23], v[218:225], 0, v191, v191 op_sel_hi:[0,0,0]
	v_mfma_scale_f32_16x16x128_f8f6f4 v[88:91], v[24:31], v[218:225], 0, v191, v191 op_sel_hi:[0,0,0]
	v_mfma_scale_f32_16x16x128_f8f6f4 v[84:87], v[16:23], v[226:233], 0, v191, v191 op_sel_hi:[0,0,0]
	v_mfma_scale_f32_16x16x128_f8f6f4 v[80:83], v[24:31], v[226:233], 0, v191, v191 op_sel_hi:[0,0,0]
	v_mfma_scale_f32_16x16x128_f8f6f4 v[76:79], v[16:23], v[234:241], 0, v191, v191 op_sel_hi:[0,0,0]
	v_mfma_scale_f32_16x16x128_f8f6f4 v[72:75], v[24:31], v[234:241], 0, v191, v191 op_sel_hi:[0,0,0]
	v_mfma_scale_f32_16x16x128_f8f6f4 v[68:71], v[16:23], v[242:249], 0, v191, v191 op_sel_hi:[0,0,0]
	v_mfma_scale_f32_16x16x128_f8f6f4 v[64:67], v[24:31], v[242:249], 0, v191, v191 op_sel_hi:[0,0,0]
	s_setprio 0
	s_mov_b32 m0, s47
	s_barrier
	ds_read_b128 v[218:221], v192 offset:16384
	ds_read_b128 v[226:229], v192 offset:18432
	ds_read_b128 v[222:225], v194 offset:16384
	ds_read_b128 v[230:233], v194 offset:18432
	ds_read_b128 v[234:237], v192 offset:20480
	ds_read_b128 v[242:245], v192 offset:22528
	ds_read_b128 v[238:241], v194 offset:20480
	ds_read_b128 v[246:249], v194 offset:22528
	global_load_lds_dwordx4 v172, s[28:29]
	s_mov_b32 m0, s83
	v_mov_b32_e32 v187, v173
	global_load_lds_dwordx4 v186, s[28:29]
	s_barrier
	s_waitcnt lgkmcnt(0)
	v_lshl_add_u64 v[188:189], s[28:29], 0, v[172:173]
	v_lshl_add_u64 v[186:187], s[28:29], 0, v[186:187]
	s_setprio 1
	s_waitcnt lgkmcnt(0)
	v_mfma_scale_f32_16x16x128_f8f6f4 v[124:127], v[0:7], v[218:225], 0, v191, v191 op_sel_hi:[0,0,0]
	v_mfma_scale_f32_16x16x128_f8f6f4 v[120:123], v[8:15], v[218:225], 0, v191, v191 op_sel_hi:[0,0,0]
	v_mfma_scale_f32_16x16x128_f8f6f4 v[116:119], v[0:7], v[226:233], 0, v191, v191 op_sel_hi:[0,0,0]
	v_mfma_scale_f32_16x16x128_f8f6f4 v[112:115], v[8:15], v[226:233], 0, v191, v191 op_sel_hi:[0,0,0]
	v_mfma_scale_f32_16x16x128_f8f6f4 v[108:111], v[0:7], v[234:241], 0, v191, v191 op_sel_hi:[0,0,0]
	v_mfma_scale_f32_16x16x128_f8f6f4 v[104:107], v[8:15], v[234:241], 0, v191, v191 op_sel_hi:[0,0,0]
	v_mfma_scale_f32_16x16x128_f8f6f4 v[100:103], v[0:7], v[242:249], 0, v191, v191 op_sel_hi:[0,0,0]
	v_mfma_scale_f32_16x16x128_f8f6f4 v[96:99], v[8:15], v[242:249], 0, v191, v191 op_sel_hi:[0,0,0]
	s_setprio 0
	s_barrier
	s_add_u32 s72, s26, 0x20000
	s_addc_u32 s73, s27, 0
	s_mov_b32 m0, s82
	v_lshl_add_u64 v[0:1], s[72:73], 0, v[162:163]
	global_load_lds_dwordx4 v[0:1], off
	v_lshl_add_u64 v[0:1], s[72:73], 0, v[164:165]
	s_mov_b32 m0, s80
	s_nop 0
	global_load_lds_dwordx4 v[0:1], off
	s_waitcnt vmcnt(6)
	s_barrier
	s_setprio 1
	v_mfma_scale_f32_16x16x128_f8f6f4 v[60:63], v[16:23], v[218:225], 0, v191, v191 op_sel_hi:[0,0,0]
	v_mfma_scale_f32_16x16x128_f8f6f4 v[56:59], v[24:31], v[218:225], 0, v191, v191 op_sel_hi:[0,0,0]
	v_mfma_scale_f32_16x16x128_f8f6f4 v[52:55], v[16:23], v[226:233], 0, v191, v191 op_sel_hi:[0,0,0]
	v_mfma_scale_f32_16x16x128_f8f6f4 v[48:51], v[24:31], v[226:233], 0, v191, v191 op_sel_hi:[0,0,0]
	v_mfma_scale_f32_16x16x128_f8f6f4 v[44:47], v[16:23], v[234:241], 0, v191, v191 op_sel_hi:[0,0,0]
	v_mfma_scale_f32_16x16x128_f8f6f4 v[40:43], v[24:31], v[234:241], 0, v191, v191 op_sel_hi:[0,0,0]
	v_mfma_scale_f32_16x16x128_f8f6f4 v[36:39], v[16:23], v[242:249], 0, v191, v191 op_sel_hi:[0,0,0]
	v_mfma_scale_f32_16x16x128_f8f6f4 v[32:35], v[24:31], v[242:249], 0, v191, v191 op_sel_hi:[0,0,0]
	s_setprio 0
	s_barrier
	ds_read_b128 v[0:3], v193 offset:32768
	ds_read_b128 v[8:11], v193 offset:34816
	ds_read_b128 v[4:7], v195 offset:32768
	ds_read_b128 v[12:15], v195 offset:34816
	s_mov_b32 m0, s81
	v_lshl_add_u64 v[180:181], s[28:29], 0, v[180:181]
	ds_read_b128 v[16:19], v192 offset:32768
	ds_read_b128 v[24:27], v192 offset:34816
	ds_read_b128 v[20:23], v194 offset:32768
	ds_read_b128 v[28:31], v194 offset:34816
	ds_read_b128 v[218:221], v192 offset:36864
	ds_read_b128 v[226:229], v192 offset:38912
	ds_read_b128 v[222:225], v194 offset:36864
	ds_read_b128 v[230:233], v194 offset:38912
	global_load_lds_dwordx4 v[180:181], off
	v_lshl_add_u64 v[178:179], s[28:29], 0, v[178:179]
	s_mov_b32 m0, s50
	s_nop 0
	global_load_lds_dwordx4 v[178:179], off
	s_waitcnt lgkmcnt(8)
	s_barrier
	s_waitcnt lgkmcnt(0)
	s_setprio 1
	v_mfma_scale_f32_16x16x128_f8f6f4 v[156:159], v[0:7], v[16:23], v[156:159], v191, v191 op_sel_hi:[0,0,0]
	v_mfma_scale_f32_16x16x128_f8f6f4 v[152:155], v[8:15], v[16:23], v[152:155], v191, v191 op_sel_hi:[0,0,0]
	v_mfma_scale_f32_16x16x128_f8f6f4 v[148:151], v[0:7], v[24:31], v[148:151], v191, v191 op_sel_hi:[0,0,0]
	v_mfma_scale_f32_16x16x128_f8f6f4 v[144:147], v[8:15], v[24:31], v[144:147], v191, v191 op_sel_hi:[0,0,0]
	v_mfma_scale_f32_16x16x128_f8f6f4 v[140:143], v[0:7], v[218:225], v[140:143], v191, v191 op_sel_hi:[0,0,0]
	v_mfma_scale_f32_16x16x128_f8f6f4 v[136:139], v[8:15], v[218:225], v[136:139], v191, v191 op_sel_hi:[0,0,0]
	v_mfma_scale_f32_16x16x128_f8f6f4 v[132:135], v[0:7], v[226:233], v[132:135], v191, v191 op_sel_hi:[0,0,0]
	v_mfma_scale_f32_16x16x128_f8f6f4 v[128:131], v[8:15], v[226:233], v[128:131], v191, v191 op_sel_hi:[0,0,0]
	s_setprio 0
	s_barrier
	s_mov_b32 m0, s51
	v_lshl_add_u64 v[178:179], v[182:183], 0, s[40:41]
	ds_read_b128 v[234:237], v193 offset:49152
	ds_read_b128 v[242:245], v193 offset:51200
	ds_read_b128 v[238:241], v195 offset:49152
	ds_read_b128 v[246:249], v195 offset:51200
	global_load_lds_dwordx4 v[178:179], off
	v_lshl_add_u64 v[178:179], v[184:185], 0, s[40:41]
	s_mov_b32 m0, s70
	s_nop 0
	global_load_lds_dwordx4 v[178:179], off
	s_barrier
	s_waitcnt lgkmcnt(0)
	s_setprio 1
	v_mfma_scale_f32_16x16x128_f8f6f4 v[92:95], v[234:241], v[16:23], v[92:95], v191, v191 op_sel_hi:[0,0,0]
	v_mfma_scale_f32_16x16x128_f8f6f4 v[88:91], v[242:249], v[16:23], v[88:91], v191, v191 op_sel_hi:[0,0,0]
	v_mfma_scale_f32_16x16x128_f8f6f4 v[84:87], v[234:241], v[24:31], v[84:87], v191, v191 op_sel_hi:[0,0,0]
	v_mfma_scale_f32_16x16x128_f8f6f4 v[80:83], v[242:249], v[24:31], v[80:83], v191, v191 op_sel_hi:[0,0,0]
	v_mfma_scale_f32_16x16x128_f8f6f4 v[76:79], v[234:241], v[218:225], v[76:79], v191, v191 op_sel_hi:[0,0,0]
	v_mfma_scale_f32_16x16x128_f8f6f4 v[72:75], v[242:249], v[218:225], v[72:75], v191, v191 op_sel_hi:[0,0,0]
	v_mfma_scale_f32_16x16x128_f8f6f4 v[68:71], v[234:241], v[226:233], v[68:71], v191, v191 op_sel_hi:[0,0,0]
	v_mfma_scale_f32_16x16x128_f8f6f4 v[64:67], v[242:249], v[226:233], v[64:67], v191, v191 op_sel_hi:[0,0,0]
	s_setprio 0
	s_mov_b32 m0, s71
	v_lshl_add_u64 v[188:189], v[188:189], 0, s[40:41]
	s_barrier
	ds_read_b128 v[16:19], v192 offset:49152
	ds_read_b128 v[24:27], v192 offset:51200
	ds_read_b128 v[20:23], v194 offset:49152
	ds_read_b128 v[28:31], v194 offset:51200
	ds_read_b128 v[178:181], v192 offset:53248
	ds_read_b128 v[218:221], v192 offset:55296
	ds_read_b128 v[182:185], v194 offset:53248
	ds_read_b128 v[222:225], v194 offset:55296
	global_load_lds_dwordx4 v[188:189], off
	v_lshl_add_u64 v[186:187], v[186:187], 0, s[40:41]
	s_mov_b32 m0, s87
	s_nop 0
	global_load_lds_dwordx4 v[186:187], off
	s_barrier
	s_waitcnt lgkmcnt(0)
	s_setprio 1
	v_mfma_scale_f32_16x16x128_f8f6f4 v[124:127], v[0:7], v[16:23], v[124:127], v191, v191 op_sel_hi:[0,0,0]
	v_mfma_scale_f32_16x16x128_f8f6f4 v[120:123], v[8:15], v[16:23], v[120:123], v191, v191 op_sel_hi:[0,0,0]
	v_mfma_scale_f32_16x16x128_f8f6f4 v[116:119], v[0:7], v[24:31], v[116:119], v191, v191 op_sel_hi:[0,0,0]
	v_mfma_scale_f32_16x16x128_f8f6f4 v[112:115], v[8:15], v[24:31], v[112:115], v191, v191 op_sel_hi:[0,0,0]
	v_mfma_scale_f32_16x16x128_f8f6f4 v[108:111], v[0:7], v[178:185], v[108:111], v191, v191 op_sel_hi:[0,0,0]
	v_mfma_scale_f32_16x16x128_f8f6f4 v[104:107], v[8:15], v[178:185], v[104:107], v191, v191 op_sel_hi:[0,0,0]
	v_mfma_scale_f32_16x16x128_f8f6f4 v[100:103], v[0:7], v[218:225], v[100:103], v191, v191 op_sel_hi:[0,0,0]
	v_mfma_scale_f32_16x16x128_f8f6f4 v[96:99], v[8:15], v[218:225], v[96:99], v191, v191 op_sel_hi:[0,0,0]
	s_setprio 0
	s_barrier
	s_add_u32 s26, s26, 0x20080
	s_addc_u32 s27, s27, 0
	s_mov_b32 m0, s1
	v_lshl_add_u64 v[0:1], s[26:27], 0, v[162:163]
	global_load_lds_dwordx4 v[0:1], off
	v_lshl_add_u64 v[0:1], s[26:27], 0, v[164:165]
	s_mov_b32 m0, s56
	s_nop 0
	global_load_lds_dwordx4 v[0:1], off
	s_waitcnt vmcnt(6)
	s_barrier
	s_setprio 1
	v_mfma_scale_f32_16x16x128_f8f6f4 v[60:63], v[234:241], v[16:23], v[60:63], v191, v191 op_sel_hi:[0,0,0]
	v_mfma_scale_f32_16x16x128_f8f6f4 v[56:59], v[242:249], v[16:23], v[56:59], v191, v191 op_sel_hi:[0,0,0]
	v_mfma_scale_f32_16x16x128_f8f6f4 v[52:55], v[234:241], v[24:31], v[52:55], v191, v191 op_sel_hi:[0,0,0]
	v_mfma_scale_f32_16x16x128_f8f6f4 v[48:51], v[242:249], v[24:31], v[48:51], v191, v191 op_sel_hi:[0,0,0]
	v_mfma_scale_f32_16x16x128_f8f6f4 v[44:47], v[234:241], v[178:185], v[44:47], v191, v191 op_sel_hi:[0,0,0]
	v_mfma_scale_f32_16x16x128_f8f6f4 v[40:43], v[242:249], v[178:185], v[40:43], v191, v191 op_sel_hi:[0,0,0]
	v_mfma_scale_f32_16x16x128_f8f6f4 v[36:39], v[234:241], v[218:225], v[36:39], v191, v191 op_sel_hi:[0,0,0]
	v_mfma_scale_f32_16x16x128_f8f6f4 v[32:35], v[242:249], v[218:225], v[32:35], v191, v191 op_sel_hi:[0,0,0]
	s_setprio 0
	s_add_i32 s13, s13, 2
	s_add_u32 s24, s24, 0x100
	s_addc_u32 s25, s25, 0
	s_add_u32 s2, s2, 0x100
	s_addc_u32 s3, s3, 0
	s_cmp_gt_u32 s13, 5
	s_barrier
	s_branch .LBB0_539
.LBB0_538:
	ds_read_b128 v[0:3], v193
	ds_read_b128 v[8:11], v193 offset:2048
	ds_read_b128 v[4:7], v195
	ds_read_b128 v[12:15], v195 offset:2048
	s_add_u32 s15, s24, 0x80
	s_addc_u32 s23, s25, 0
	s_and_b64 s[26:27], s[26:27], exec
	s_cselect_b32 s29, s19, s23
	s_cselect_b32 s28, s18, s15
	s_cselect_b32 s27, s17, s3
	s_cselect_b32 s26, s16, s2
	v_lshl_add_u64 v[16:17], s[24:25], 0, v[168:169]
	s_add_i32 m0, s47, 0xc000
	ds_read_b128 v[218:221], v192
	ds_read_b128 v[226:229], v192 offset:2048
	ds_read_b128 v[222:225], v194
	ds_read_b128 v[230:233], v194 offset:2048
	ds_read_b128 v[234:237], v192 offset:4096
	ds_read_b128 v[242:245], v192 offset:6144
	ds_read_b128 v[238:241], v194 offset:4096
	ds_read_b128 v[246:249], v194 offset:6144
	global_load_lds_dwordx4 v[16:17], off
	v_lshl_add_u64 v[16:17], s[24:25], 0, v[174:175]
	s_add_i32 m0, s47, 0xe000
	s_nop 0
	global_load_lds_dwordx4 v[16:17], off
	s_waitcnt lgkmcnt(8)
	s_barrier
	s_waitcnt lgkmcnt(0)
	s_setprio 1
	v_mfma_scale_f32_16x16x128_f8f6f4 v[156:159], v[0:7], v[218:225], v[156:159], v191, v191 op_sel_hi:[0,0,0]
	v_mfma_scale_f32_16x16x128_f8f6f4 v[152:155], v[8:15], v[218:225], v[152:155], v191, v191 op_sel_hi:[0,0,0]
	v_mfma_scale_f32_16x16x128_f8f6f4 v[148:151], v[0:7], v[226:233], v[148:151], v191, v191 op_sel_hi:[0,0,0]
	v_mfma_scale_f32_16x16x128_f8f6f4 v[144:147], v[8:15], v[226:233], v[144:147], v191, v191 op_sel_hi:[0,0,0]
	v_mfma_scale_f32_16x16x128_f8f6f4 v[140:143], v[0:7], v[234:241], v[140:143], v191, v191 op_sel_hi:[0,0,0]
	v_mfma_scale_f32_16x16x128_f8f6f4 v[136:139], v[8:15], v[234:241], v[136:139], v191, v191 op_sel_hi:[0,0,0]
	v_mfma_scale_f32_16x16x128_f8f6f4 v[132:135], v[0:7], v[242:249], v[132:135], v191, v191 op_sel_hi:[0,0,0]
	v_mfma_scale_f32_16x16x128_f8f6f4 v[128:131], v[8:15], v[242:249], v[128:131], v191, v191 op_sel_hi:[0,0,0]
	s_setprio 0
	s_barrier
	s_mov_b32 m0, s30
	v_lshl_add_u64 v[182:183], s[26:27], 0, v[162:163]
	ds_read_b128 v[16:19], v193 offset:16384
	ds_read_b128 v[24:27], v193 offset:18432
	ds_read_b128 v[20:23], v195 offset:16384
	ds_read_b128 v[28:31], v195 offset:18432
	global_load_lds_dwordx4 v[182:183], off
	v_lshl_add_u64 v[184:185], s[26:27], 0, v[164:165]
	s_mov_b32 m0, s46
	s_nop 0
	global_load_lds_dwordx4 v[184:185], off
	s_barrier
	s_waitcnt lgkmcnt(0)
	s_setprio 1
	v_mfma_scale_f32_16x16x128_f8f6f4 v[92:95], v[16:23], v[218:225], v[92:95], v191, v191 op_sel_hi:[0,0,0]
	v_mfma_scale_f32_16x16x128_f8f6f4 v[88:91], v[24:31], v[218:225], v[88:91], v191, v191 op_sel_hi:[0,0,0]
	v_mfma_scale_f32_16x16x128_f8f6f4 v[84:87], v[16:23], v[226:233], v[84:87], v191, v191 op_sel_hi:[0,0,0]
	v_mfma_scale_f32_16x16x128_f8f6f4 v[80:83], v[24:31], v[226:233], v[80:83], v191, v191 op_sel_hi:[0,0,0]
	v_mfma_scale_f32_16x16x128_f8f6f4 v[76:79], v[16:23], v[234:241], v[76:79], v191, v191 op_sel_hi:[0,0,0]
	v_mfma_scale_f32_16x16x128_f8f6f4 v[72:75], v[24:31], v[234:241], v[72:75], v191, v191 op_sel_hi:[0,0,0]
	v_mfma_scale_f32_16x16x128_f8f6f4 v[68:71], v[16:23], v[242:249], v[68:71], v191, v191 op_sel_hi:[0,0,0]
	v_mfma_scale_f32_16x16x128_f8f6f4 v[64:67], v[24:31], v[242:249], v[64:67], v191, v191 op_sel_hi:[0,0,0]
	s_setprio 0
	s_mov_b32 m0, s47
	s_barrier
	ds_read_b128 v[218:221], v192 offset:16384
	ds_read_b128 v[226:229], v192 offset:18432
	ds_read_b128 v[222:225], v194 offset:16384
	ds_read_b128 v[230:233], v194 offset:18432
	ds_read_b128 v[234:237], v192 offset:20480
	ds_read_b128 v[242:245], v192 offset:22528
	ds_read_b128 v[238:241], v194 offset:20480
	ds_read_b128 v[246:249], v194 offset:22528
	global_load_lds_dwordx4 v172, s[28:29]
	s_mov_b32 m0, s83
	v_mov_b32_e32 v187, v173
	global_load_lds_dwordx4 v186, s[28:29]
	s_barrier
	s_waitcnt lgkmcnt(0)
	v_lshl_add_u64 v[188:189], s[28:29], 0, v[172:173]
	v_lshl_add_u64 v[186:187], s[28:29], 0, v[186:187]
	s_setprio 1
	s_waitcnt lgkmcnt(0)
	v_mfma_scale_f32_16x16x128_f8f6f4 v[124:127], v[0:7], v[218:225], v[124:127], v191, v191 op_sel_hi:[0,0,0]
	v_mfma_scale_f32_16x16x128_f8f6f4 v[120:123], v[8:15], v[218:225], v[120:123], v191, v191 op_sel_hi:[0,0,0]
	v_mfma_scale_f32_16x16x128_f8f6f4 v[116:119], v[0:7], v[226:233], v[116:119], v191, v191 op_sel_hi:[0,0,0]
	v_mfma_scale_f32_16x16x128_f8f6f4 v[112:115], v[8:15], v[226:233], v[112:115], v191, v191 op_sel_hi:[0,0,0]
	v_mfma_scale_f32_16x16x128_f8f6f4 v[108:111], v[0:7], v[234:241], v[108:111], v191, v191 op_sel_hi:[0,0,0]
	v_mfma_scale_f32_16x16x128_f8f6f4 v[104:107], v[8:15], v[234:241], v[104:107], v191, v191 op_sel_hi:[0,0,0]
	v_mfma_scale_f32_16x16x128_f8f6f4 v[100:103], v[0:7], v[242:249], v[100:103], v191, v191 op_sel_hi:[0,0,0]
	v_mfma_scale_f32_16x16x128_f8f6f4 v[96:99], v[8:15], v[242:249], v[96:99], v191, v191 op_sel_hi:[0,0,0]
	s_setprio 0
	s_barrier
	s_add_u32 s72, s26, 0x20000
	s_addc_u32 s73, s27, 0
	s_mov_b32 m0, s82
	v_lshl_add_u64 v[0:1], s[72:73], 0, v[162:163]
	global_load_lds_dwordx4 v[0:1], off
	v_lshl_add_u64 v[0:1], s[72:73], 0, v[164:165]
	s_mov_b32 m0, s80
	s_nop 0
	global_load_lds_dwordx4 v[0:1], off
	s_waitcnt vmcnt(6)
	s_barrier
	s_setprio 1
	v_mfma_scale_f32_16x16x128_f8f6f4 v[60:63], v[16:23], v[218:225], v[60:63], v191, v191 op_sel_hi:[0,0,0]
	v_mfma_scale_f32_16x16x128_f8f6f4 v[56:59], v[24:31], v[218:225], v[56:59], v191, v191 op_sel_hi:[0,0,0]
	v_mfma_scale_f32_16x16x128_f8f6f4 v[52:55], v[16:23], v[226:233], v[52:55], v191, v191 op_sel_hi:[0,0,0]
	v_mfma_scale_f32_16x16x128_f8f6f4 v[48:51], v[24:31], v[226:233], v[48:51], v191, v191 op_sel_hi:[0,0,0]
	v_mfma_scale_f32_16x16x128_f8f6f4 v[44:47], v[16:23], v[234:241], v[44:47], v191, v191 op_sel_hi:[0,0,0]
	v_mfma_scale_f32_16x16x128_f8f6f4 v[40:43], v[24:31], v[234:241], v[40:43], v191, v191 op_sel_hi:[0,0,0]
	v_mfma_scale_f32_16x16x128_f8f6f4 v[36:39], v[16:23], v[242:249], v[36:39], v191, v191 op_sel_hi:[0,0,0]
	v_mfma_scale_f32_16x16x128_f8f6f4 v[32:35], v[24:31], v[242:249], v[32:35], v191, v191 op_sel_hi:[0,0,0]
	s_setprio 0
	s_barrier
	ds_read_b128 v[0:3], v193 offset:32768
	ds_read_b128 v[8:11], v193 offset:34816
	ds_read_b128 v[4:7], v195 offset:32768
	ds_read_b128 v[12:15], v195 offset:34816
	s_mov_b32 m0, s81
	v_lshl_add_u64 v[180:181], s[28:29], 0, v[180:181]
	ds_read_b128 v[16:19], v192 offset:32768
	ds_read_b128 v[24:27], v192 offset:34816
	ds_read_b128 v[20:23], v194 offset:32768
	ds_read_b128 v[28:31], v194 offset:34816
	ds_read_b128 v[218:221], v192 offset:36864
	ds_read_b128 v[226:229], v192 offset:38912
	ds_read_b128 v[222:225], v194 offset:36864
	ds_read_b128 v[230:233], v194 offset:38912
	global_load_lds_dwordx4 v[180:181], off
	v_lshl_add_u64 v[178:179], s[28:29], 0, v[178:179]
	s_mov_b32 m0, s50
	s_nop 0
	global_load_lds_dwordx4 v[178:179], off
	s_waitcnt lgkmcnt(8)
	s_barrier
	s_waitcnt lgkmcnt(0)
	s_setprio 1
	v_mfma_scale_f32_16x16x128_f8f6f4 v[156:159], v[0:7], v[16:23], v[156:159], v191, v191 op_sel_hi:[0,0,0]
	v_mfma_scale_f32_16x16x128_f8f6f4 v[152:155], v[8:15], v[16:23], v[152:155], v191, v191 op_sel_hi:[0,0,0]
	v_mfma_scale_f32_16x16x128_f8f6f4 v[148:151], v[0:7], v[24:31], v[148:151], v191, v191 op_sel_hi:[0,0,0]
	v_mfma_scale_f32_16x16x128_f8f6f4 v[144:147], v[8:15], v[24:31], v[144:147], v191, v191 op_sel_hi:[0,0,0]
	v_mfma_scale_f32_16x16x128_f8f6f4 v[140:143], v[0:7], v[218:225], v[140:143], v191, v191 op_sel_hi:[0,0,0]
	v_mfma_scale_f32_16x16x128_f8f6f4 v[136:139], v[8:15], v[218:225], v[136:139], v191, v191 op_sel_hi:[0,0,0]
	v_mfma_scale_f32_16x16x128_f8f6f4 v[132:135], v[0:7], v[226:233], v[132:135], v191, v191 op_sel_hi:[0,0,0]
	v_mfma_scale_f32_16x16x128_f8f6f4 v[128:131], v[8:15], v[226:233], v[128:131], v191, v191 op_sel_hi:[0,0,0]
	s_setprio 0
	s_barrier
	s_mov_b32 m0, s51
	v_lshl_add_u64 v[178:179], v[182:183], 0, s[40:41]
	ds_read_b128 v[234:237], v193 offset:49152
	ds_read_b128 v[242:245], v193 offset:51200
	ds_read_b128 v[238:241], v195 offset:49152
	ds_read_b128 v[246:249], v195 offset:51200
	global_load_lds_dwordx4 v[178:179], off
	v_lshl_add_u64 v[178:179], v[184:185], 0, s[40:41]
	s_mov_b32 m0, s70
	s_nop 0
	global_load_lds_dwordx4 v[178:179], off
	s_barrier
	s_waitcnt lgkmcnt(0)
	s_setprio 1
	v_mfma_scale_f32_16x16x128_f8f6f4 v[92:95], v[234:241], v[16:23], v[92:95], v191, v191 op_sel_hi:[0,0,0]
	v_mfma_scale_f32_16x16x128_f8f6f4 v[88:91], v[242:249], v[16:23], v[88:91], v191, v191 op_sel_hi:[0,0,0]
	v_mfma_scale_f32_16x16x128_f8f6f4 v[84:87], v[234:241], v[24:31], v[84:87], v191, v191 op_sel_hi:[0,0,0]
	v_mfma_scale_f32_16x16x128_f8f6f4 v[80:83], v[242:249], v[24:31], v[80:83], v191, v191 op_sel_hi:[0,0,0]
	v_mfma_scale_f32_16x16x128_f8f6f4 v[76:79], v[234:241], v[218:225], v[76:79], v191, v191 op_sel_hi:[0,0,0]
	v_mfma_scale_f32_16x16x128_f8f6f4 v[72:75], v[242:249], v[218:225], v[72:75], v191, v191 op_sel_hi:[0,0,0]
	v_mfma_scale_f32_16x16x128_f8f6f4 v[68:71], v[234:241], v[226:233], v[68:71], v191, v191 op_sel_hi:[0,0,0]
	v_mfma_scale_f32_16x16x128_f8f6f4 v[64:67], v[242:249], v[226:233], v[64:67], v191, v191 op_sel_hi:[0,0,0]
	s_setprio 0
	s_mov_b32 m0, s71
	v_lshl_add_u64 v[188:189], v[188:189], 0, s[40:41]
	s_barrier
	ds_read_b128 v[16:19], v192 offset:49152
	ds_read_b128 v[24:27], v192 offset:51200
	ds_read_b128 v[20:23], v194 offset:49152
	ds_read_b128 v[28:31], v194 offset:51200
	ds_read_b128 v[178:181], v192 offset:53248
	ds_read_b128 v[218:221], v192 offset:55296
	ds_read_b128 v[182:185], v194 offset:53248
	ds_read_b128 v[222:225], v194 offset:55296
	global_load_lds_dwordx4 v[188:189], off
	v_lshl_add_u64 v[186:187], v[186:187], 0, s[40:41]
	s_mov_b32 m0, s87
	s_nop 0
	global_load_lds_dwordx4 v[186:187], off
	s_barrier
	s_waitcnt lgkmcnt(0)
	s_setprio 1
	v_mfma_scale_f32_16x16x128_f8f6f4 v[124:127], v[0:7], v[16:23], v[124:127], v191, v191 op_sel_hi:[0,0,0]
	v_mfma_scale_f32_16x16x128_f8f6f4 v[120:123], v[8:15], v[16:23], v[120:123], v191, v191 op_sel_hi:[0,0,0]
	v_mfma_scale_f32_16x16x128_f8f6f4 v[116:119], v[0:7], v[24:31], v[116:119], v191, v191 op_sel_hi:[0,0,0]
	v_mfma_scale_f32_16x16x128_f8f6f4 v[112:115], v[8:15], v[24:31], v[112:115], v191, v191 op_sel_hi:[0,0,0]
	v_mfma_scale_f32_16x16x128_f8f6f4 v[108:111], v[0:7], v[178:185], v[108:111], v191, v191 op_sel_hi:[0,0,0]
	v_mfma_scale_f32_16x16x128_f8f6f4 v[104:107], v[8:15], v[178:185], v[104:107], v191, v191 op_sel_hi:[0,0,0]
	v_mfma_scale_f32_16x16x128_f8f6f4 v[100:103], v[0:7], v[218:225], v[100:103], v191, v191 op_sel_hi:[0,0,0]
	v_mfma_scale_f32_16x16x128_f8f6f4 v[96:99], v[8:15], v[218:225], v[96:99], v191, v191 op_sel_hi:[0,0,0]
	s_setprio 0
	s_barrier
	s_add_u32 s26, s26, 0x20080
	s_addc_u32 s27, s27, 0
	s_mov_b32 m0, s1
	v_lshl_add_u64 v[0:1], s[26:27], 0, v[162:163]
	global_load_lds_dwordx4 v[0:1], off
	v_lshl_add_u64 v[0:1], s[26:27], 0, v[164:165]
	s_mov_b32 m0, s56
	s_nop 0
	global_load_lds_dwordx4 v[0:1], off
	s_waitcnt vmcnt(6)
	s_barrier
	s_setprio 1
	v_mfma_scale_f32_16x16x128_f8f6f4 v[60:63], v[234:241], v[16:23], v[60:63], v191, v191 op_sel_hi:[0,0,0]
	v_mfma_scale_f32_16x16x128_f8f6f4 v[56:59], v[242:249], v[16:23], v[56:59], v191, v191 op_sel_hi:[0,0,0]
	v_mfma_scale_f32_16x16x128_f8f6f4 v[52:55], v[234:241], v[24:31], v[52:55], v191, v191 op_sel_hi:[0,0,0]
	v_mfma_scale_f32_16x16x128_f8f6f4 v[48:51], v[242:249], v[24:31], v[48:51], v191, v191 op_sel_hi:[0,0,0]
	v_mfma_scale_f32_16x16x128_f8f6f4 v[44:47], v[234:241], v[178:185], v[44:47], v191, v191 op_sel_hi:[0,0,0]
	v_mfma_scale_f32_16x16x128_f8f6f4 v[40:43], v[242:249], v[178:185], v[40:43], v191, v191 op_sel_hi:[0,0,0]
	v_mfma_scale_f32_16x16x128_f8f6f4 v[36:39], v[234:241], v[218:225], v[36:39], v191, v191 op_sel_hi:[0,0,0]
	v_mfma_scale_f32_16x16x128_f8f6f4 v[32:35], v[242:249], v[218:225], v[32:35], v191, v191 op_sel_hi:[0,0,0]
	s_setprio 0
	s_add_i32 s13, s13, 2
	s_add_u32 s24, s24, 0x100
	s_addc_u32 s25, s25, 0
	s_add_u32 s2, s2, 0x100
	s_addc_u32 s3, s3, 0
	s_cmp_gt_u32 s13, 5
	s_barrier
	s_cbranch_scc1 .LBB0_541

.Lpeel_out:
	s_mov_b64 s[28:29], 0
	v_mov_b64_e32 v[136:137], v[132:133]
	v_mov_b64_e32 v[138:139], v[128:129]
	v_mov_b32_e32 v172, v130
	v_mov_b32_e32 v140, v134
	ds_read_b128 v[142:145], v186
	ds_read_b128 v[146:149], v186 offset:1024
	ds_read_b128 v[150:153], v186 offset:2048
	ds_read_b128 v[162:165], v186 offset:3072
	s_add_u32 s30, s26, 0x80
	s_addc_u32 s31, s27, 0
	s_and_b64 s[28:29], s[28:29], exec
	s_cselect_b32 s31, s19, s31
	s_cselect_b32 s30, s18, s30
	s_cselect_b32 s29, s17, s15
	s_cselect_b32 s28, s16, s9
	v_lshl_add_u64 v[154:155], s[26:27], 0, v[128:129]
	s_add_i32 m0, s23, 0xc000
	ds_read_b128 v[166:169], v185
	ds_read_b128 v[174:177], v185 offset:1024
	ds_read_b128 v[178:181], v185 offset:2048
	ds_read_b128 v[204:207], v185 offset:3072
	ds_read_b128 v[208:211], v185 offset:4096
	ds_read_b128 v[214:217], v185 offset:5120
	ds_read_b128 v[218:221], v185 offset:6144
	ds_read_b128 v[222:225], v185 offset:7168
	global_load_lds_dwordx4 v[154:155], off
	v_lshl_add_u64 v[154:155], s[26:27], 0, v[132:133]
	s_add_i32 m0, s23, 0xe000
	s_nop 0
	global_load_lds_dwordx4 v[154:155], off
	s_waitcnt lgkmcnt(8)
	s_barrier
	s_waitcnt lgkmcnt(0)
	s_setprio 1
	v_mfma_f32_16x16x32_bf16 v[124:127], v[142:145], v[166:169], 0
	v_mfma_f32_16x16x32_bf16 v[120:123], v[150:153], v[166:169], 0
	v_mfma_f32_16x16x32_bf16 v[116:119], v[142:145], v[178:181], 0
	v_mfma_f32_16x16x32_bf16 v[112:115], v[150:153], v[178:181], 0
	v_mfma_f32_16x16x32_bf16 v[108:111], v[142:145], v[208:211], 0
	v_mfma_f32_16x16x32_bf16 v[104:107], v[150:153], v[208:211], 0
	v_mfma_f32_16x16x32_bf16 v[100:103], v[142:145], v[218:221], 0
	v_mfma_f32_16x16x32_bf16 v[96:99], v[150:153], v[218:221], 0
	v_mfma_f32_16x16x32_bf16 v[124:127], v[146:149], v[174:177], v[124:127]
	v_mfma_f32_16x16x32_bf16 v[120:123], v[162:165], v[174:177], v[120:123]
	v_mfma_f32_16x16x32_bf16 v[116:119], v[146:149], v[204:207], v[116:119]
	v_mfma_f32_16x16x32_bf16 v[112:115], v[162:165], v[204:207], v[112:115]
	v_mfma_f32_16x16x32_bf16 v[108:111], v[146:149], v[214:217], v[108:111]
	v_mfma_f32_16x16x32_bf16 v[104:107], v[162:165], v[214:217], v[104:107]
	v_mfma_f32_16x16x32_bf16 v[100:103], v[146:149], v[222:225], v[100:103]
	v_mfma_f32_16x16x32_bf16 v[96:99], v[162:165], v[222:225], v[96:99]
	s_setprio 0
	s_barrier
	s_mov_b32 m0, s25
	v_lshl_add_u64 v[170:171], s[28:29], 0, v[158:159]
	ds_read_b128 v[226:229], v186 offset:16384
	ds_read_b128 v[230:233], v186 offset:17408
	ds_read_b128 v[234:237], v186 offset:18432
	ds_read_b128 v[238:241], v186 offset:19456
	global_load_lds_dwordx4 v[170:171], off
	v_lshl_add_u64 v[182:183], s[28:29], 0, v[160:161]
	s_mov_b32 m0, s51
	s_nop 0
	global_load_lds_dwordx4 v[182:183], off
	s_barrier
	s_waitcnt lgkmcnt(0)
	s_setprio 1
	v_mfma_f32_16x16x32_bf16 v[68:71], v[226:229], v[166:169], 0
	v_mfma_f32_16x16x32_bf16 v[64:67], v[234:237], v[166:169], 0
	v_mfma_f32_16x16x32_bf16 v[52:55], v[226:229], v[178:181], 0
	v_mfma_f32_16x16x32_bf16 v[48:51], v[234:237], v[178:181], 0
	v_mfma_f32_16x16x32_bf16 v[44:47], v[226:229], v[208:211], 0
	v_mfma_f32_16x16x32_bf16 v[40:43], v[234:237], v[208:211], 0
	v_mfma_f32_16x16x32_bf16 v[36:39], v[226:229], v[218:221], 0
	v_mfma_f32_16x16x32_bf16 v[32:35], v[234:237], v[218:221], 0
	v_mfma_f32_16x16x32_bf16 v[68:71], v[230:233], v[174:177], v[68:71]
	v_mfma_f32_16x16x32_bf16 v[64:67], v[238:241], v[174:177], v[64:67]
	v_mfma_f32_16x16x32_bf16 v[52:55], v[230:233], v[204:207], v[52:55]
	v_mfma_f32_16x16x32_bf16 v[48:51], v[238:241], v[204:207], v[48:51]
	v_mfma_f32_16x16x32_bf16 v[44:47], v[230:233], v[214:217], v[44:47]
	v_mfma_f32_16x16x32_bf16 v[40:43], v[238:241], v[214:217], v[40:43]
	v_mfma_f32_16x16x32_bf16 v[36:39], v[230:233], v[222:225], v[36:39]
	v_mfma_f32_16x16x32_bf16 v[32:35], v[238:241], v[222:225], v[32:35]
	s_setprio 0
	s_mov_b32 m0, s23
	s_barrier
	ds_read_b128 v[166:169], v185 offset:16384
	ds_read_b128 v[174:177], v185 offset:17408
	ds_read_b128 v[178:181], v185 offset:18432
	ds_read_b128 v[204:207], v185 offset:19456
	ds_read_b128 v[208:211], v185 offset:20480
	ds_read_b128 v[214:217], v185 offset:21504
	ds_read_b128 v[218:221], v185 offset:22528
	ds_read_b128 v[222:225], v185 offset:23552
	global_load_lds_dwordx4 v172, s[30:31]
	s_mov_b32 m0, s56
	v_mov_b32_e32 v141, v173
	global_load_lds_dwordx4 v140, s[30:31]
	s_barrier
	s_waitcnt lgkmcnt(0)
	v_lshl_add_u64 v[196:197], s[30:31], 0, v[172:173]
	v_lshl_add_u64 v[242:243], s[30:31], 0, v[140:141]
	s_setprio 1
	s_waitcnt lgkmcnt(0)
	v_mfma_f32_16x16x32_bf16 v[92:95], v[142:145], v[166:169], 0
	v_mfma_f32_16x16x32_bf16 v[88:91], v[150:153], v[166:169], 0
	v_mfma_f32_16x16x32_bf16 v[84:87], v[142:145], v[178:181], 0
	v_mfma_f32_16x16x32_bf16 v[80:83], v[150:153], v[178:181], 0
	v_mfma_f32_16x16x32_bf16 v[76:79], v[142:145], v[208:211], 0
	v_mfma_f32_16x16x32_bf16 v[72:75], v[150:153], v[208:211], 0
	v_mfma_f32_16x16x32_bf16 v[60:63], v[142:145], v[218:221], 0
	v_mfma_f32_16x16x32_bf16 v[56:59], v[150:153], v[218:221], 0
	v_mfma_f32_16x16x32_bf16 v[92:95], v[146:149], v[174:177], v[92:95]
	v_mfma_f32_16x16x32_bf16 v[88:91], v[162:165], v[174:177], v[88:91]
	v_mfma_f32_16x16x32_bf16 v[84:87], v[146:149], v[204:207], v[84:87]
	v_mfma_f32_16x16x32_bf16 v[80:83], v[162:165], v[204:207], v[80:83]
	v_mfma_f32_16x16x32_bf16 v[76:79], v[146:149], v[214:217], v[76:79]
	v_mfma_f32_16x16x32_bf16 v[72:75], v[162:165], v[214:217], v[72:75]
	v_mfma_f32_16x16x32_bf16 v[60:63], v[146:149], v[222:225], v[60:63]
	v_mfma_f32_16x16x32_bf16 v[56:59], v[162:165], v[222:225], v[56:59]
	s_setprio 0
	s_barrier
	s_add_u32 s94, s28, 0x40000
	s_addc_u32 s95, s29, 0
	s_mov_b32 m0, s65
	v_lshl_add_u64 v[140:141], s[94:95], 0, v[158:159]
	global_load_lds_dwordx4 v[140:141], off
	v_lshl_add_u64 v[140:141], s[94:95], 0, v[160:161]
	s_mov_b32 m0, s70
	s_nop 0
	global_load_lds_dwordx4 v[140:141], off
	s_waitcnt vmcnt(6)
	s_barrier
	s_setprio 1
	v_mfma_f32_16x16x32_bf16 v[28:31], v[226:229], v[166:169], 0
	v_mfma_f32_16x16x32_bf16 v[24:27], v[234:237], v[166:169], 0
	v_mfma_f32_16x16x32_bf16 v[20:23], v[226:229], v[178:181], 0
	v_mfma_f32_16x16x32_bf16 v[16:19], v[234:237], v[178:181], 0
	v_mfma_f32_16x16x32_bf16 v[12:15], v[226:229], v[208:211], 0
	v_mfma_f32_16x16x32_bf16 v[8:11], v[234:237], v[208:211], 0
	v_mfma_f32_16x16x32_bf16 v[4:7], v[226:229], v[218:221], 0
	v_mfma_f32_16x16x32_bf16 v[0:3], v[234:237], v[218:221], 0
	v_mfma_f32_16x16x32_bf16 v[28:31], v[230:233], v[174:177], v[28:31]
	v_mfma_f32_16x16x32_bf16 v[24:27], v[238:241], v[174:177], v[24:27]
	v_mfma_f32_16x16x32_bf16 v[20:23], v[230:233], v[204:207], v[20:23]
	v_mfma_f32_16x16x32_bf16 v[16:19], v[238:241], v[204:207], v[16:19]
	v_mfma_f32_16x16x32_bf16 v[12:15], v[230:233], v[214:217], v[12:15]
	v_mfma_f32_16x16x32_bf16 v[8:11], v[238:241], v[214:217], v[8:11]
	v_mfma_f32_16x16x32_bf16 v[4:7], v[230:233], v[222:225], v[4:7]
	v_mfma_f32_16x16x32_bf16 v[0:3], v[238:241], v[222:225], v[0:3]
	s_setprio 0
	s_barrier
	ds_read_b128 v[140:143], v186 offset:32768
	ds_read_b128 v[144:147], v186 offset:33792
	ds_read_b128 v[148:151], v186 offset:34816
	ds_read_b128 v[152:155], v186 offset:35840
	s_mov_b32 m0, s71
	v_lshl_add_u64 v[138:139], s[30:31], 0, v[138:139]
	ds_read_b128 v[162:165], v185 offset:32768
	ds_read_b128 v[166:169], v185 offset:33792
	ds_read_b128 v[174:177], v185 offset:34816
	ds_read_b128 v[178:181], v185 offset:35840
	ds_read_b128 v[204:207], v185 offset:36864
	ds_read_b128 v[208:211], v185 offset:37888
	ds_read_b128 v[214:217], v185 offset:38912
	ds_read_b128 v[218:221], v185 offset:39936
	global_load_lds_dwordx4 v[138:139], off
	v_lshl_add_u64 v[136:137], s[30:31], 0, v[136:137]
	s_mov_b32 m0, s80
	s_nop 0
	global_load_lds_dwordx4 v[136:137], off
	s_waitcnt lgkmcnt(8)
	s_barrier
	s_waitcnt lgkmcnt(0)
	s_setprio 1
	v_mfma_f32_16x16x32_bf16 v[124:127], v[140:143], v[162:165], v[124:127]
	v_mfma_f32_16x16x32_bf16 v[120:123], v[148:151], v[162:165], v[120:123]
	v_mfma_f32_16x16x32_bf16 v[116:119], v[140:143], v[174:177], v[116:119]
	v_mfma_f32_16x16x32_bf16 v[112:115], v[148:151], v[174:177], v[112:115]
	v_mfma_f32_16x16x32_bf16 v[108:111], v[140:143], v[204:207], v[108:111]
	v_mfma_f32_16x16x32_bf16 v[104:107], v[148:151], v[204:207], v[104:107]
	v_mfma_f32_16x16x32_bf16 v[100:103], v[140:143], v[214:217], v[100:103]
	v_mfma_f32_16x16x32_bf16 v[96:99], v[148:151], v[214:217], v[96:99]
	v_mfma_f32_16x16x32_bf16 v[124:127], v[144:147], v[166:169], v[124:127]
	v_mfma_f32_16x16x32_bf16 v[120:123], v[152:155], v[166:169], v[120:123]
	v_mfma_f32_16x16x32_bf16 v[116:119], v[144:147], v[178:181], v[116:119]
	v_mfma_f32_16x16x32_bf16 v[112:115], v[152:155], v[178:181], v[112:115]
	v_mfma_f32_16x16x32_bf16 v[108:111], v[144:147], v[208:211], v[108:111]
	v_mfma_f32_16x16x32_bf16 v[104:107], v[152:155], v[208:211], v[104:107]
	v_mfma_f32_16x16x32_bf16 v[100:103], v[144:147], v[218:221], v[100:103]
	v_mfma_f32_16x16x32_bf16 v[96:99], v[152:155], v[218:221], v[96:99]
	s_setprio 0
	s_barrier
	s_mov_b32 m0, s81
	v_lshl_add_u64 v[170:171], v[170:171], 0, s[40:41]
	ds_read_b128 v[136:139], v186 offset:49152
	ds_read_b128 v[222:225], v186 offset:50176
	ds_read_b128 v[226:229], v186 offset:51200
	ds_read_b128 v[230:233], v186 offset:52224
	global_load_lds_dwordx4 v[170:171], off
	v_lshl_add_u64 v[170:171], v[182:183], 0, s[40:41]
	s_mov_b32 m0, s82
	s_nop 0
	global_load_lds_dwordx4 v[170:171], off
	s_barrier
	s_waitcnt lgkmcnt(0)
	s_setprio 1
	v_mfma_f32_16x16x32_bf16 v[68:71], v[136:139], v[162:165], v[68:71]
	v_mfma_f32_16x16x32_bf16 v[64:67], v[226:229], v[162:165], v[64:67]
	v_mfma_f32_16x16x32_bf16 v[52:55], v[136:139], v[174:177], v[52:55]
	v_mfma_f32_16x16x32_bf16 v[48:51], v[226:229], v[174:177], v[48:51]
	v_mfma_f32_16x16x32_bf16 v[44:47], v[136:139], v[204:207], v[44:47]
	v_mfma_f32_16x16x32_bf16 v[40:43], v[226:229], v[204:207], v[40:43]
	v_mfma_f32_16x16x32_bf16 v[36:39], v[136:139], v[214:217], v[36:39]
	v_mfma_f32_16x16x32_bf16 v[32:35], v[226:229], v[214:217], v[32:35]
	v_mfma_f32_16x16x32_bf16 v[68:71], v[222:225], v[166:169], v[68:71]
	v_mfma_f32_16x16x32_bf16 v[64:67], v[230:233], v[166:169], v[64:67]
	v_mfma_f32_16x16x32_bf16 v[52:55], v[222:225], v[178:181], v[52:55]
	v_mfma_f32_16x16x32_bf16 v[48:51], v[230:233], v[178:181], v[48:51]
	v_mfma_f32_16x16x32_bf16 v[44:47], v[222:225], v[208:211], v[44:47]
	v_mfma_f32_16x16x32_bf16 v[40:43], v[230:233], v[208:211], v[40:43]
	v_mfma_f32_16x16x32_bf16 v[36:39], v[222:225], v[218:221], v[36:39]
	v_mfma_f32_16x16x32_bf16 v[32:35], v[230:233], v[218:221], v[32:35]
	s_setprio 0
	s_mov_b32 m0, s83
	v_lshl_add_u64 v[170:171], v[196:197], 0, s[40:41]
	s_barrier
	ds_read_b128 v[162:165], v185 offset:49152
	ds_read_b128 v[166:169], v185 offset:50176
	ds_read_b128 v[174:177], v185 offset:51200
	ds_read_b128 v[178:181], v185 offset:52224
	ds_read_b128 v[204:207], v185 offset:53248
	ds_read_b128 v[208:211], v185 offset:54272
	ds_read_b128 v[214:217], v185 offset:55296
	ds_read_b128 v[218:221], v185 offset:56320
	global_load_lds_dwordx4 v[170:171], off
	v_lshl_add_u64 v[170:171], v[242:243], 0, s[40:41]
	s_mov_b32 m0, s85
	s_nop 0
	global_load_lds_dwordx4 v[170:171], off
	s_barrier
	s_waitcnt lgkmcnt(0)
	s_setprio 1
	v_mfma_f32_16x16x32_bf16 v[92:95], v[140:143], v[162:165], v[92:95]
	v_mfma_f32_16x16x32_bf16 v[88:91], v[148:151], v[162:165], v[88:91]
	v_mfma_f32_16x16x32_bf16 v[84:87], v[140:143], v[174:177], v[84:87]
	v_mfma_f32_16x16x32_bf16 v[80:83], v[148:151], v[174:177], v[80:83]
	v_mfma_f32_16x16x32_bf16 v[76:79], v[140:143], v[204:207], v[76:79]
	v_mfma_f32_16x16x32_bf16 v[72:75], v[148:151], v[204:207], v[72:75]
	v_mfma_f32_16x16x32_bf16 v[60:63], v[140:143], v[214:217], v[60:63]
	v_mfma_f32_16x16x32_bf16 v[56:59], v[148:151], v[214:217], v[56:59]
	v_mfma_f32_16x16x32_bf16 v[92:95], v[144:147], v[166:169], v[92:95]
	v_mfma_f32_16x16x32_bf16 v[88:91], v[152:155], v[166:169], v[88:91]
	v_mfma_f32_16x16x32_bf16 v[84:87], v[144:147], v[178:181], v[84:87]
	v_mfma_f32_16x16x32_bf16 v[80:83], v[152:155], v[178:181], v[80:83]
	v_mfma_f32_16x16x32_bf16 v[76:79], v[144:147], v[208:211], v[76:79]
	v_mfma_f32_16x16x32_bf16 v[72:75], v[152:155], v[208:211], v[72:75]
	v_mfma_f32_16x16x32_bf16 v[60:63], v[144:147], v[218:221], v[60:63]
	v_mfma_f32_16x16x32_bf16 v[56:59], v[152:155], v[218:221], v[56:59]
	s_setprio 0
	s_barrier
	s_add_u32 s28, s28, 0x40080
	s_addc_u32 s29, s29, 0
	s_mov_b32 m0, s87
	v_lshl_add_u64 v[140:141], s[28:29], 0, v[158:159]
	global_load_lds_dwordx4 v[140:141], off
	v_lshl_add_u64 v[140:141], s[28:29], 0, v[160:161]
	s_mov_b32 m0, s44
	s_nop 0
	global_load_lds_dwordx4 v[140:141], off
	s_waitcnt vmcnt(6)
	s_barrier
	s_setprio 1
	v_mfma_f32_16x16x32_bf16 v[28:31], v[136:139], v[162:165], v[28:31]
	v_mfma_f32_16x16x32_bf16 v[24:27], v[226:229], v[162:165], v[24:27]
	v_mfma_f32_16x16x32_bf16 v[20:23], v[136:139], v[174:177], v[20:23]
	v_mfma_f32_16x16x32_bf16 v[16:19], v[226:229], v[174:177], v[16:19]
	v_mfma_f32_16x16x32_bf16 v[12:15], v[136:139], v[204:207], v[12:15]
	v_mfma_f32_16x16x32_bf16 v[8:11], v[226:229], v[204:207], v[8:11]
	v_mfma_f32_16x16x32_bf16 v[4:7], v[136:139], v[214:217], v[4:7]
	v_mfma_f32_16x16x32_bf16 v[0:3], v[226:229], v[214:217], v[0:3]
	v_mfma_f32_16x16x32_bf16 v[28:31], v[222:225], v[166:169], v[28:31]
	v_mfma_f32_16x16x32_bf16 v[24:27], v[230:233], v[166:169], v[24:27]
	v_mfma_f32_16x16x32_bf16 v[20:23], v[222:225], v[178:181], v[20:23]
	v_mfma_f32_16x16x32_bf16 v[16:19], v[230:233], v[178:181], v[16:19]
	v_mfma_f32_16x16x32_bf16 v[12:15], v[222:225], v[208:211], v[12:15]
	v_mfma_f32_16x16x32_bf16 v[8:11], v[230:233], v[208:211], v[8:11]
	v_mfma_f32_16x16x32_bf16 v[4:7], v[222:225], v[218:221], v[4:7]
	v_mfma_f32_16x16x32_bf16 v[0:3], v[230:233], v[218:221], v[0:3]
	s_setprio 0
	s_add_i32 vcc_lo, vcc_lo, 2
	s_add_u32 s26, s26, 0x100
	s_addc_u32 s27, s27, 0
	s_add_u32 s9, s9, 0x100
	s_addc_u32 s15, s15, 0
	s_cmp_gt_u32 vcc_lo, 13
	s_barrier
	s_branch .LBB0_1320
.LBB0_1319:
	ds_read_b128 v[142:145], v186
	ds_read_b128 v[146:149], v186 offset:1024
	ds_read_b128 v[150:153], v186 offset:2048
	ds_read_b128 v[162:165], v186 offset:3072
	s_add_u32 s30, s26, 0x80
	s_addc_u32 s31, s27, 0
	s_and_b64 s[28:29], s[28:29], exec
	s_cselect_b32 s31, s19, s31
	s_cselect_b32 s30, s18, s30
	s_cselect_b32 s29, s17, s15
	s_cselect_b32 s28, s16, s9
	v_lshl_add_u64 v[154:155], s[26:27], 0, v[128:129]
	s_add_i32 m0, s23, 0xc000
	ds_read_b128 v[166:169], v185
	ds_read_b128 v[174:177], v185 offset:1024
	ds_read_b128 v[178:181], v185 offset:2048
	ds_read_b128 v[204:207], v185 offset:3072
	ds_read_b128 v[208:211], v185 offset:4096
	ds_read_b128 v[214:217], v185 offset:5120
	ds_read_b128 v[218:221], v185 offset:6144
	ds_read_b128 v[222:225], v185 offset:7168
	global_load_lds_dwordx4 v[154:155], off
	v_lshl_add_u64 v[154:155], s[26:27], 0, v[132:133]
	s_add_i32 m0, s23, 0xe000
	s_nop 0
	global_load_lds_dwordx4 v[154:155], off
	s_waitcnt lgkmcnt(8)
	s_barrier
	s_waitcnt lgkmcnt(0)
	s_setprio 1
	v_mfma_f32_16x16x32_bf16 v[124:127], v[142:145], v[166:169], v[124:127]
	v_mfma_f32_16x16x32_bf16 v[120:123], v[150:153], v[166:169], v[120:123]
	v_mfma_f32_16x16x32_bf16 v[116:119], v[142:145], v[178:181], v[116:119]
	v_mfma_f32_16x16x32_bf16 v[112:115], v[150:153], v[178:181], v[112:115]
	v_mfma_f32_16x16x32_bf16 v[108:111], v[142:145], v[208:211], v[108:111]
	v_mfma_f32_16x16x32_bf16 v[104:107], v[150:153], v[208:211], v[104:107]
	v_mfma_f32_16x16x32_bf16 v[100:103], v[142:145], v[218:221], v[100:103]
	v_mfma_f32_16x16x32_bf16 v[96:99], v[150:153], v[218:221], v[96:99]
	v_mfma_f32_16x16x32_bf16 v[124:127], v[146:149], v[174:177], v[124:127]
	v_mfma_f32_16x16x32_bf16 v[120:123], v[162:165], v[174:177], v[120:123]
	v_mfma_f32_16x16x32_bf16 v[116:119], v[146:149], v[204:207], v[116:119]
	v_mfma_f32_16x16x32_bf16 v[112:115], v[162:165], v[204:207], v[112:115]
	v_mfma_f32_16x16x32_bf16 v[108:111], v[146:149], v[214:217], v[108:111]
	v_mfma_f32_16x16x32_bf16 v[104:107], v[162:165], v[214:217], v[104:107]
	v_mfma_f32_16x16x32_bf16 v[100:103], v[146:149], v[222:225], v[100:103]
	v_mfma_f32_16x16x32_bf16 v[96:99], v[162:165], v[222:225], v[96:99]
	s_setprio 0
	s_barrier
	s_mov_b32 m0, s25
	v_lshl_add_u64 v[170:171], s[28:29], 0, v[158:159]
	ds_read_b128 v[226:229], v186 offset:16384
	ds_read_b128 v[230:233], v186 offset:17408
	ds_read_b128 v[234:237], v186 offset:18432
	ds_read_b128 v[238:241], v186 offset:19456
	global_load_lds_dwordx4 v[170:171], off
	v_lshl_add_u64 v[182:183], s[28:29], 0, v[160:161]
	s_mov_b32 m0, s51
	s_nop 0
	global_load_lds_dwordx4 v[182:183], off
	s_barrier
	s_waitcnt lgkmcnt(0)
	s_setprio 1
	v_mfma_f32_16x16x32_bf16 v[68:71], v[226:229], v[166:169], v[68:71]
	v_mfma_f32_16x16x32_bf16 v[64:67], v[234:237], v[166:169], v[64:67]
	v_mfma_f32_16x16x32_bf16 v[52:55], v[226:229], v[178:181], v[52:55]
	v_mfma_f32_16x16x32_bf16 v[48:51], v[234:237], v[178:181], v[48:51]
	v_mfma_f32_16x16x32_bf16 v[44:47], v[226:229], v[208:211], v[44:47]
	v_mfma_f32_16x16x32_bf16 v[40:43], v[234:237], v[208:211], v[40:43]
	v_mfma_f32_16x16x32_bf16 v[36:39], v[226:229], v[218:221], v[36:39]
	v_mfma_f32_16x16x32_bf16 v[32:35], v[234:237], v[218:221], v[32:35]
	v_mfma_f32_16x16x32_bf16 v[68:71], v[230:233], v[174:177], v[68:71]
	v_mfma_f32_16x16x32_bf16 v[64:67], v[238:241], v[174:177], v[64:67]
	v_mfma_f32_16x16x32_bf16 v[52:55], v[230:233], v[204:207], v[52:55]
	v_mfma_f32_16x16x32_bf16 v[48:51], v[238:241], v[204:207], v[48:51]
	v_mfma_f32_16x16x32_bf16 v[44:47], v[230:233], v[214:217], v[44:47]
	v_mfma_f32_16x16x32_bf16 v[40:43], v[238:241], v[214:217], v[40:43]
	v_mfma_f32_16x16x32_bf16 v[36:39], v[230:233], v[222:225], v[36:39]
	v_mfma_f32_16x16x32_bf16 v[32:35], v[238:241], v[222:225], v[32:35]
	s_setprio 0
	s_mov_b32 m0, s23
	s_barrier
	ds_read_b128 v[166:169], v185 offset:16384
	ds_read_b128 v[174:177], v185 offset:17408
	ds_read_b128 v[178:181], v185 offset:18432
	ds_read_b128 v[204:207], v185 offset:19456
	ds_read_b128 v[208:211], v185 offset:20480
	ds_read_b128 v[214:217], v185 offset:21504
	ds_read_b128 v[218:221], v185 offset:22528
	ds_read_b128 v[222:225], v185 offset:23552
	global_load_lds_dwordx4 v172, s[30:31]
	s_mov_b32 m0, s56
	v_mov_b32_e32 v141, v173
	global_load_lds_dwordx4 v140, s[30:31]
	s_barrier
	s_waitcnt lgkmcnt(0)
	v_lshl_add_u64 v[196:197], s[30:31], 0, v[172:173]
	v_lshl_add_u64 v[242:243], s[30:31], 0, v[140:141]
	s_setprio 1
	s_waitcnt lgkmcnt(0)
	v_mfma_f32_16x16x32_bf16 v[92:95], v[142:145], v[166:169], v[92:95]
	v_mfma_f32_16x16x32_bf16 v[88:91], v[150:153], v[166:169], v[88:91]
	v_mfma_f32_16x16x32_bf16 v[84:87], v[142:145], v[178:181], v[84:87]
	v_mfma_f32_16x16x32_bf16 v[80:83], v[150:153], v[178:181], v[80:83]
	v_mfma_f32_16x16x32_bf16 v[76:79], v[142:145], v[208:211], v[76:79]
	v_mfma_f32_16x16x32_bf16 v[72:75], v[150:153], v[208:211], v[72:75]
	v_mfma_f32_16x16x32_bf16 v[60:63], v[142:145], v[218:221], v[60:63]
	v_mfma_f32_16x16x32_bf16 v[56:59], v[150:153], v[218:221], v[56:59]
	v_mfma_f32_16x16x32_bf16 v[92:95], v[146:149], v[174:177], v[92:95]
	v_mfma_f32_16x16x32_bf16 v[88:91], v[162:165], v[174:177], v[88:91]
	v_mfma_f32_16x16x32_bf16 v[84:87], v[146:149], v[204:207], v[84:87]
	v_mfma_f32_16x16x32_bf16 v[80:83], v[162:165], v[204:207], v[80:83]
	v_mfma_f32_16x16x32_bf16 v[76:79], v[146:149], v[214:217], v[76:79]
	v_mfma_f32_16x16x32_bf16 v[72:75], v[162:165], v[214:217], v[72:75]
	v_mfma_f32_16x16x32_bf16 v[60:63], v[146:149], v[222:225], v[60:63]
	v_mfma_f32_16x16x32_bf16 v[56:59], v[162:165], v[222:225], v[56:59]
	s_setprio 0
	s_barrier
	s_add_u32 s94, s28, 0x40000
	s_addc_u32 s95, s29, 0
	s_mov_b32 m0, s65
	v_lshl_add_u64 v[140:141], s[94:95], 0, v[158:159]
	global_load_lds_dwordx4 v[140:141], off
	v_lshl_add_u64 v[140:141], s[94:95], 0, v[160:161]
	s_mov_b32 m0, s70
	s_nop 0
	global_load_lds_dwordx4 v[140:141], off
	s_waitcnt vmcnt(6)
	s_barrier
	s_setprio 1
	v_mfma_f32_16x16x32_bf16 v[28:31], v[226:229], v[166:169], v[28:31]
	v_mfma_f32_16x16x32_bf16 v[24:27], v[234:237], v[166:169], v[24:27]
	v_mfma_f32_16x16x32_bf16 v[20:23], v[226:229], v[178:181], v[20:23]
	v_mfma_f32_16x16x32_bf16 v[16:19], v[234:237], v[178:181], v[16:19]
	v_mfma_f32_16x16x32_bf16 v[12:15], v[226:229], v[208:211], v[12:15]
	v_mfma_f32_16x16x32_bf16 v[8:11], v[234:237], v[208:211], v[8:11]
	v_mfma_f32_16x16x32_bf16 v[4:7], v[226:229], v[218:221], v[4:7]
	v_mfma_f32_16x16x32_bf16 v[0:3], v[234:237], v[218:221], v[0:3]
	v_mfma_f32_16x16x32_bf16 v[28:31], v[230:233], v[174:177], v[28:31]
	v_mfma_f32_16x16x32_bf16 v[24:27], v[238:241], v[174:177], v[24:27]
	v_mfma_f32_16x16x32_bf16 v[20:23], v[230:233], v[204:207], v[20:23]
	v_mfma_f32_16x16x32_bf16 v[16:19], v[238:241], v[204:207], v[16:19]
	v_mfma_f32_16x16x32_bf16 v[12:15], v[230:233], v[214:217], v[12:15]
	v_mfma_f32_16x16x32_bf16 v[8:11], v[238:241], v[214:217], v[8:11]
	v_mfma_f32_16x16x32_bf16 v[4:7], v[230:233], v[222:225], v[4:7]
	v_mfma_f32_16x16x32_bf16 v[0:3], v[238:241], v[222:225], v[0:3]
	s_setprio 0
	s_barrier
	ds_read_b128 v[140:143], v186 offset:32768
	ds_read_b128 v[144:147], v186 offset:33792
	ds_read_b128 v[148:151], v186 offset:34816
	ds_read_b128 v[152:155], v186 offset:35840
	s_mov_b32 m0, s71
	v_lshl_add_u64 v[138:139], s[30:31], 0, v[138:139]
	ds_read_b128 v[162:165], v185 offset:32768
	ds_read_b128 v[166:169], v185 offset:33792
	ds_read_b128 v[174:177], v185 offset:34816
	ds_read_b128 v[178:181], v185 offset:35840
	ds_read_b128 v[204:207], v185 offset:36864
	ds_read_b128 v[208:211], v185 offset:37888
	ds_read_b128 v[214:217], v185 offset:38912
	ds_read_b128 v[218:221], v185 offset:39936
	global_load_lds_dwordx4 v[138:139], off
	v_lshl_add_u64 v[136:137], s[30:31], 0, v[136:137]
	s_mov_b32 m0, s80
	s_nop 0
	global_load_lds_dwordx4 v[136:137], off
	s_waitcnt lgkmcnt(8)
	s_barrier
	s_waitcnt lgkmcnt(0)
	s_setprio 1
	v_mfma_f32_16x16x32_bf16 v[124:127], v[140:143], v[162:165], v[124:127]
	v_mfma_f32_16x16x32_bf16 v[120:123], v[148:151], v[162:165], v[120:123]
	v_mfma_f32_16x16x32_bf16 v[116:119], v[140:143], v[174:177], v[116:119]
	v_mfma_f32_16x16x32_bf16 v[112:115], v[148:151], v[174:177], v[112:115]
	v_mfma_f32_16x16x32_bf16 v[108:111], v[140:143], v[204:207], v[108:111]
	v_mfma_f32_16x16x32_bf16 v[104:107], v[148:151], v[204:207], v[104:107]
	v_mfma_f32_16x16x32_bf16 v[100:103], v[140:143], v[214:217], v[100:103]
	v_mfma_f32_16x16x32_bf16 v[96:99], v[148:151], v[214:217], v[96:99]
	v_mfma_f32_16x16x32_bf16 v[124:127], v[144:147], v[166:169], v[124:127]
	v_mfma_f32_16x16x32_bf16 v[120:123], v[152:155], v[166:169], v[120:123]
	v_mfma_f32_16x16x32_bf16 v[116:119], v[144:147], v[178:181], v[116:119]
	v_mfma_f32_16x16x32_bf16 v[112:115], v[152:155], v[178:181], v[112:115]
	v_mfma_f32_16x16x32_bf16 v[108:111], v[144:147], v[208:211], v[108:111]
	v_mfma_f32_16x16x32_bf16 v[104:107], v[152:155], v[208:211], v[104:107]
	v_mfma_f32_16x16x32_bf16 v[100:103], v[144:147], v[218:221], v[100:103]
	v_mfma_f32_16x16x32_bf16 v[96:99], v[152:155], v[218:221], v[96:99]
	s_setprio 0
	s_barrier
	s_mov_b32 m0, s81
	v_lshl_add_u64 v[170:171], v[170:171], 0, s[40:41]
	ds_read_b128 v[136:139], v186 offset:49152
	ds_read_b128 v[222:225], v186 offset:50176
	ds_read_b128 v[226:229], v186 offset:51200
	ds_read_b128 v[230:233], v186 offset:52224
	global_load_lds_dwordx4 v[170:171], off
	v_lshl_add_u64 v[170:171], v[182:183], 0, s[40:41]
	s_mov_b32 m0, s82
	s_nop 0
	global_load_lds_dwordx4 v[170:171], off
	s_barrier
	s_waitcnt lgkmcnt(0)
	s_setprio 1
	v_mfma_f32_16x16x32_bf16 v[68:71], v[136:139], v[162:165], v[68:71]
	v_mfma_f32_16x16x32_bf16 v[64:67], v[226:229], v[162:165], v[64:67]
	v_mfma_f32_16x16x32_bf16 v[52:55], v[136:139], v[174:177], v[52:55]
	v_mfma_f32_16x16x32_bf16 v[48:51], v[226:229], v[174:177], v[48:51]
	v_mfma_f32_16x16x32_bf16 v[44:47], v[136:139], v[204:207], v[44:47]
	v_mfma_f32_16x16x32_bf16 v[40:43], v[226:229], v[204:207], v[40:43]
	v_mfma_f32_16x16x32_bf16 v[36:39], v[136:139], v[214:217], v[36:39]
	v_mfma_f32_16x16x32_bf16 v[32:35], v[226:229], v[214:217], v[32:35]
	v_mfma_f32_16x16x32_bf16 v[68:71], v[222:225], v[166:169], v[68:71]
	v_mfma_f32_16x16x32_bf16 v[64:67], v[230:233], v[166:169], v[64:67]
	v_mfma_f32_16x16x32_bf16 v[52:55], v[222:225], v[178:181], v[52:55]
	v_mfma_f32_16x16x32_bf16 v[48:51], v[230:233], v[178:181], v[48:51]
	v_mfma_f32_16x16x32_bf16 v[44:47], v[222:225], v[208:211], v[44:47]
	v_mfma_f32_16x16x32_bf16 v[40:43], v[230:233], v[208:211], v[40:43]
	v_mfma_f32_16x16x32_bf16 v[36:39], v[222:225], v[218:221], v[36:39]
	v_mfma_f32_16x16x32_bf16 v[32:35], v[230:233], v[218:221], v[32:35]
	s_setprio 0
	s_mov_b32 m0, s83
	v_lshl_add_u64 v[170:171], v[196:197], 0, s[40:41]
	s_barrier
	ds_read_b128 v[162:165], v185 offset:49152
	ds_read_b128 v[166:169], v185 offset:50176
	ds_read_b128 v[174:177], v185 offset:51200
	ds_read_b128 v[178:181], v185 offset:52224
	ds_read_b128 v[204:207], v185 offset:53248
	ds_read_b128 v[208:211], v185 offset:54272
	ds_read_b128 v[214:217], v185 offset:55296
	ds_read_b128 v[218:221], v185 offset:56320
	global_load_lds_dwordx4 v[170:171], off
	v_lshl_add_u64 v[170:171], v[242:243], 0, s[40:41]
	s_mov_b32 m0, s85
	s_nop 0
	global_load_lds_dwordx4 v[170:171], off
	s_barrier
	s_waitcnt lgkmcnt(0)
	s_setprio 1
	v_mfma_f32_16x16x32_bf16 v[92:95], v[140:143], v[162:165], v[92:95]
	v_mfma_f32_16x16x32_bf16 v[88:91], v[148:151], v[162:165], v[88:91]
	v_mfma_f32_16x16x32_bf16 v[84:87], v[140:143], v[174:177], v[84:87]
	v_mfma_f32_16x16x32_bf16 v[80:83], v[148:151], v[174:177], v[80:83]
	v_mfma_f32_16x16x32_bf16 v[76:79], v[140:143], v[204:207], v[76:79]
	v_mfma_f32_16x16x32_bf16 v[72:75], v[148:151], v[204:207], v[72:75]
	v_mfma_f32_16x16x32_bf16 v[60:63], v[140:143], v[214:217], v[60:63]
	v_mfma_f32_16x16x32_bf16 v[56:59], v[148:151], v[214:217], v[56:59]
	v_mfma_f32_16x16x32_bf16 v[92:95], v[144:147], v[166:169], v[92:95]
	v_mfma_f32_16x16x32_bf16 v[88:91], v[152:155], v[166:169], v[88:91]
	v_mfma_f32_16x16x32_bf16 v[84:87], v[144:147], v[178:181], v[84:87]
	v_mfma_f32_16x16x32_bf16 v[80:83], v[152:155], v[178:181], v[80:83]
	v_mfma_f32_16x16x32_bf16 v[76:79], v[144:147], v[208:211], v[76:79]
	v_mfma_f32_16x16x32_bf16 v[72:75], v[152:155], v[208:211], v[72:75]
	v_mfma_f32_16x16x32_bf16 v[60:63], v[144:147], v[218:221], v[60:63]
	v_mfma_f32_16x16x32_bf16 v[56:59], v[152:155], v[218:221], v[56:59]
	s_setprio 0
	s_barrier
	s_add_u32 s28, s28, 0x40080
	s_addc_u32 s29, s29, 0
	s_mov_b32 m0, s87
	v_lshl_add_u64 v[140:141], s[28:29], 0, v[158:159]
	global_load_lds_dwordx4 v[140:141], off
	v_lshl_add_u64 v[140:141], s[28:29], 0, v[160:161]
	s_mov_b32 m0, s44
	s_nop 0
	global_load_lds_dwordx4 v[140:141], off
	s_waitcnt vmcnt(6)
	s_barrier
	s_setprio 1
	v_mfma_f32_16x16x32_bf16 v[28:31], v[136:139], v[162:165], v[28:31]
	v_mfma_f32_16x16x32_bf16 v[24:27], v[226:229], v[162:165], v[24:27]
	v_mfma_f32_16x16x32_bf16 v[20:23], v[136:139], v[174:177], v[20:23]
	v_mfma_f32_16x16x32_bf16 v[16:19], v[226:229], v[174:177], v[16:19]
	v_mfma_f32_16x16x32_bf16 v[12:15], v[136:139], v[204:207], v[12:15]
	v_mfma_f32_16x16x32_bf16 v[8:11], v[226:229], v[204:207], v[8:11]
	v_mfma_f32_16x16x32_bf16 v[4:7], v[136:139], v[214:217], v[4:7]
	v_mfma_f32_16x16x32_bf16 v[0:3], v[226:229], v[214:217], v[0:3]
	v_mfma_f32_16x16x32_bf16 v[28:31], v[222:225], v[166:169], v[28:31]
	v_mfma_f32_16x16x32_bf16 v[24:27], v[230:233], v[166:169], v[24:27]
	v_mfma_f32_16x16x32_bf16 v[20:23], v[222:225], v[178:181], v[20:23]
	v_mfma_f32_16x16x32_bf16 v[16:19], v[230:233], v[178:181], v[16:19]
	v_mfma_f32_16x16x32_bf16 v[12:15], v[222:225], v[208:211], v[12:15]
	v_mfma_f32_16x16x32_bf16 v[8:11], v[230:233], v[208:211], v[8:11]
	v_mfma_f32_16x16x32_bf16 v[4:7], v[222:225], v[218:221], v[4:7]
	v_mfma_f32_16x16x32_bf16 v[0:3], v[230:233], v[218:221], v[0:3]
	s_setprio 0
	s_add_i32 vcc_lo, vcc_lo, 2
	s_add_u32 s26, s26, 0x100
	s_addc_u32 s27, s27, 0
	s_add_u32 s9, s9, 0x100
	s_addc_u32 s15, s15, 0
	s_cmp_gt_u32 vcc_lo, 13
	s_barrier
	s_cbranch_scc1 .LBB0_1303

.Lpeel_gu:
	s_mov_b64 s[24:25], 0
	v_mov_b32_e32 v186, v166
	v_mov_b32_e32 v184, v170
	v_mov_b64_e32 v[178:179], v[168:169]
	v_mov_b64_e32 v[176:177], v[174:175]
	ds_read_b128 v[0:3], v191
	ds_read_b128 v[8:11], v191 offset:2048
	ds_read_b128 v[4:7], v193
	ds_read_b128 v[12:15], v193 offset:2048
	s_add_u32 s26, s22, 0x80
	s_addc_u32 s27, s23, 0
	s_and_b64 s[24:25], s[24:25], exec
	s_cselect_b32 s27, s19, s27
	s_cselect_b32 s26, s18, s26
	s_cselect_b32 s25, s17, s3
	s_cselect_b32 s24, s16, s2
	v_lshl_add_u64 v[16:17], s[22:23], 0, v[168:169]
	s_add_i32 m0, s44, 0xc000
	ds_read_b128 v[226:229], v190
	ds_read_b128 v[234:237], v190 offset:2048
	ds_read_b128 v[230:233], v192
	ds_read_b128 v[238:241], v192 offset:2048
	ds_read_b128 v[242:245], v190 offset:4096
	ds_read_b128 v[204:207], v190 offset:6144
	ds_read_b128 v[246:249], v192 offset:4096
	ds_read_b128 v[208:211], v192 offset:6144
	global_load_lds_dwordx4 v[16:17], off
	v_lshl_add_u64 v[16:17], s[22:23], 0, v[174:175]
	s_add_i32 m0, s44, 0xe000
	s_nop 0
	global_load_lds_dwordx4 v[16:17], off
	s_waitcnt lgkmcnt(8)
	s_barrier
	s_waitcnt lgkmcnt(0)
	s_setprio 1
	v_mfma_scale_f32_16x16x128_f8f6f4 v[156:159], v[0:7], v[226:233], 0, v189, v189 op_sel_hi:[0,0,0]
	v_mfma_scale_f32_16x16x128_f8f6f4 v[148:151], v[8:15], v[226:233], 0, v189, v189 op_sel_hi:[0,0,0]
	v_mfma_scale_f32_16x16x128_f8f6f4 v[140:143], v[0:7], v[234:241], 0, v189, v189 op_sel_hi:[0,0,0]
	v_mfma_scale_f32_16x16x128_f8f6f4 v[132:135], v[8:15], v[234:241], 0, v189, v189 op_sel_hi:[0,0,0]
	v_mfma_scale_f32_16x16x128_f8f6f4 v[124:127], v[0:7], v[242:249], 0, v189, v189 op_sel_hi:[0,0,0]
	v_mfma_scale_f32_16x16x128_f8f6f4 v[116:119], v[8:15], v[242:249], 0, v189, v189 op_sel_hi:[0,0,0]
	v_mfma_scale_f32_16x16x128_f8f6f4 v[108:111], v[0:7], v[204:211], 0, v189, v189 op_sel_hi:[0,0,0]
	v_mfma_scale_f32_16x16x128_f8f6f4 v[100:103], v[8:15], v[204:211], 0, v189, v189 op_sel_hi:[0,0,0]
	s_setprio 0
	s_barrier
	s_mov_b32 m0, s46
	v_lshl_add_u64 v[180:181], s[24:25], 0, v[160:161]
	ds_read_b128 v[16:19], v191 offset:16384
	ds_read_b128 v[24:27], v191 offset:18432
	ds_read_b128 v[20:23], v193 offset:16384
	ds_read_b128 v[28:31], v193 offset:18432
	global_load_lds_dwordx4 v[180:181], off
	v_lshl_add_u64 v[182:183], s[24:25], 0, v[162:163]
	s_mov_b32 m0, s47
	s_nop 0
	global_load_lds_dwordx4 v[182:183], off
	s_barrier
	s_waitcnt lgkmcnt(0)
	s_setprio 1
	v_mfma_scale_f32_16x16x128_f8f6f4 v[152:155], v[16:23], v[226:233], 0, v189, v189 op_sel_hi:[0,0,0]
	v_mfma_scale_f32_16x16x128_f8f6f4 v[144:147], v[24:31], v[226:233], 0, v189, v189 op_sel_hi:[0,0,0]
	v_mfma_scale_f32_16x16x128_f8f6f4 v[136:139], v[16:23], v[234:241], 0, v189, v189 op_sel_hi:[0,0,0]
	v_mfma_scale_f32_16x16x128_f8f6f4 v[128:131], v[24:31], v[234:241], 0, v189, v189 op_sel_hi:[0,0,0]
	v_mfma_scale_f32_16x16x128_f8f6f4 v[120:123], v[16:23], v[242:249], 0, v189, v189 op_sel_hi:[0,0,0]
	v_mfma_scale_f32_16x16x128_f8f6f4 v[112:115], v[24:31], v[242:249], 0, v189, v189 op_sel_hi:[0,0,0]
	v_mfma_scale_f32_16x16x128_f8f6f4 v[104:107], v[16:23], v[204:211], 0, v189, v189 op_sel_hi:[0,0,0]
	v_mfma_scale_f32_16x16x128_f8f6f4 v[96:99], v[24:31], v[204:211], 0, v189, v189 op_sel_hi:[0,0,0]
	s_setprio 0
	s_mov_b32 m0, s44
	s_barrier
	ds_read_b128 v[204:207], v190 offset:16384
	ds_read_b128 v[226:229], v190 offset:18432
	ds_read_b128 v[208:211], v192 offset:16384
	ds_read_b128 v[230:233], v192 offset:18432
	ds_read_b128 v[234:237], v190 offset:20480
	ds_read_b128 v[242:245], v190 offset:22528
	ds_read_b128 v[238:241], v192 offset:20480
	ds_read_b128 v[246:249], v192 offset:22528
	global_load_lds_dwordx4 v186, s[26:27]
	s_mov_b32 m0, s50
	v_mov_b32_e32 v187, v173
	global_load_lds_dwordx4 v184, s[26:27]
	s_barrier
	s_waitcnt lgkmcnt(0)
	v_mov_b32_e32 v185, v173
	v_lshl_add_u64 v[186:187], s[26:27], 0, v[186:187]
	v_lshl_add_u64 v[184:185], s[26:27], 0, v[184:185]
	s_setprio 1
	s_waitcnt lgkmcnt(0)
	v_mfma_scale_f32_16x16x128_f8f6f4 v[92:95], v[0:7], v[204:211], 0, v189, v189 op_sel_hi:[0,0,0]
	v_mfma_scale_f32_16x16x128_f8f6f4 v[84:87], v[8:15], v[204:211], 0, v189, v189 op_sel_hi:[0,0,0]
	v_mfma_scale_f32_16x16x128_f8f6f4 v[76:79], v[0:7], v[226:233], 0, v189, v189 op_sel_hi:[0,0,0]
	v_mfma_scale_f32_16x16x128_f8f6f4 v[68:71], v[8:15], v[226:233], 0, v189, v189 op_sel_hi:[0,0,0]
	v_mfma_scale_f32_16x16x128_f8f6f4 v[60:63], v[0:7], v[234:241], 0, v189, v189 op_sel_hi:[0,0,0]
	v_mfma_scale_f32_16x16x128_f8f6f4 v[52:55], v[8:15], v[234:241], 0, v189, v189 op_sel_hi:[0,0,0]
	v_mfma_scale_f32_16x16x128_f8f6f4 v[44:47], v[0:7], v[242:249], 0, v189, v189 op_sel_hi:[0,0,0]
	v_mfma_scale_f32_16x16x128_f8f6f4 v[36:39], v[8:15], v[242:249], 0, v189, v189 op_sel_hi:[0,0,0]
	s_setprio 0
	s_barrier
	s_add_u32 s72, s24, 0x20000
	s_addc_u32 s73, s25, 0
	s_mov_b32 m0, s51
	v_lshl_add_u64 v[0:1], s[72:73], 0, v[160:161]
	global_load_lds_dwordx4 v[0:1], off
	v_lshl_add_u64 v[0:1], s[72:73], 0, v[162:163]
	s_mov_b32 m0, s56
	s_nop 0
	global_load_lds_dwordx4 v[0:1], off
	s_waitcnt vmcnt(6)
	s_barrier
	s_setprio 1
	v_mfma_scale_f32_16x16x128_f8f6f4 v[88:91], v[16:23], v[204:211], 0, v189, v189 op_sel_hi:[0,0,0]
	v_mfma_scale_f32_16x16x128_f8f6f4 v[80:83], v[24:31], v[204:211], 0, v189, v189 op_sel_hi:[0,0,0]
	v_mfma_scale_f32_16x16x128_f8f6f4 v[72:75], v[16:23], v[226:233], 0, v189, v189 op_sel_hi:[0,0,0]
	v_mfma_scale_f32_16x16x128_f8f6f4 v[64:67], v[24:31], v[226:233], 0, v189, v189 op_sel_hi:[0,0,0]
	v_mfma_scale_f32_16x16x128_f8f6f4 v[56:59], v[16:23], v[234:241], 0, v189, v189 op_sel_hi:[0,0,0]
	v_mfma_scale_f32_16x16x128_f8f6f4 v[48:51], v[24:31], v[234:241], 0, v189, v189 op_sel_hi:[0,0,0]
	v_mfma_scale_f32_16x16x128_f8f6f4 v[40:43], v[16:23], v[242:249], 0, v189, v189 op_sel_hi:[0,0,0]
	v_mfma_scale_f32_16x16x128_f8f6f4 v[32:35], v[24:31], v[242:249], 0, v189, v189 op_sel_hi:[0,0,0]
	s_setprio 0
	s_barrier
	ds_read_b128 v[0:3], v191 offset:32768
	ds_read_b128 v[8:11], v191 offset:34816
	ds_read_b128 v[4:7], v193 offset:32768
	ds_read_b128 v[12:15], v193 offset:34816
	s_mov_b32 m0, s65
	v_lshl_add_u64 v[178:179], s[26:27], 0, v[178:179]
	ds_read_b128 v[16:19], v190 offset:32768
	ds_read_b128 v[24:27], v190 offset:34816
	ds_read_b128 v[20:23], v192 offset:32768
	ds_read_b128 v[28:31], v192 offset:34816
	ds_read_b128 v[204:207], v190 offset:36864
	ds_read_b128 v[226:229], v190 offset:38912
	ds_read_b128 v[208:211], v192 offset:36864
	ds_read_b128 v[230:233], v192 offset:38912
	global_load_lds_dwordx4 v[178:179], off
	v_lshl_add_u64 v[176:177], s[26:27], 0, v[176:177]
	s_mov_b32 m0, s70
	s_nop 0
	global_load_lds_dwordx4 v[176:177], off
	s_waitcnt lgkmcnt(8)
	s_barrier
	s_waitcnt lgkmcnt(0)
	s_setprio 1
	v_mfma_scale_f32_16x16x128_f8f6f4 v[156:159], v[0:7], v[16:23], v[156:159], v189, v189 op_sel_hi:[0,0,0]
	v_mfma_scale_f32_16x16x128_f8f6f4 v[148:151], v[8:15], v[16:23], v[148:151], v189, v189 op_sel_hi:[0,0,0]
	v_mfma_scale_f32_16x16x128_f8f6f4 v[140:143], v[0:7], v[24:31], v[140:143], v189, v189 op_sel_hi:[0,0,0]
	v_mfma_scale_f32_16x16x128_f8f6f4 v[132:135], v[8:15], v[24:31], v[132:135], v189, v189 op_sel_hi:[0,0,0]
	v_mfma_scale_f32_16x16x128_f8f6f4 v[124:127], v[0:7], v[204:211], v[124:127], v189, v189 op_sel_hi:[0,0,0]
	v_mfma_scale_f32_16x16x128_f8f6f4 v[116:119], v[8:15], v[204:211], v[116:119], v189, v189 op_sel_hi:[0,0,0]
	v_mfma_scale_f32_16x16x128_f8f6f4 v[108:111], v[0:7], v[226:233], v[108:111], v189, v189 op_sel_hi:[0,0,0]
	v_mfma_scale_f32_16x16x128_f8f6f4 v[100:103], v[8:15], v[226:233], v[100:103], v189, v189 op_sel_hi:[0,0,0]
	s_setprio 0
	s_barrier
	s_mov_b32 m0, s71
	v_lshl_add_u64 v[176:177], v[180:181], 0, s[40:41]
	ds_read_b128 v[234:237], v191 offset:49152
	ds_read_b128 v[242:245], v191 offset:51200
	ds_read_b128 v[238:241], v193 offset:49152
	ds_read_b128 v[246:249], v193 offset:51200
	global_load_lds_dwordx4 v[176:177], off
	v_lshl_add_u64 v[176:177], v[182:183], 0, s[40:41]
	s_mov_b32 m0, s80
	s_nop 0
	global_load_lds_dwordx4 v[176:177], off
	s_barrier
	s_waitcnt lgkmcnt(0)
	s_setprio 1
	v_mfma_scale_f32_16x16x128_f8f6f4 v[152:155], v[234:241], v[16:23], v[152:155], v189, v189 op_sel_hi:[0,0,0]
	v_mfma_scale_f32_16x16x128_f8f6f4 v[144:147], v[242:249], v[16:23], v[144:147], v189, v189 op_sel_hi:[0,0,0]
	v_mfma_scale_f32_16x16x128_f8f6f4 v[136:139], v[234:241], v[24:31], v[136:139], v189, v189 op_sel_hi:[0,0,0]
	v_mfma_scale_f32_16x16x128_f8f6f4 v[128:131], v[242:249], v[24:31], v[128:131], v189, v189 op_sel_hi:[0,0,0]
	v_mfma_scale_f32_16x16x128_f8f6f4 v[120:123], v[234:241], v[204:211], v[120:123], v189, v189 op_sel_hi:[0,0,0]
	v_mfma_scale_f32_16x16x128_f8f6f4 v[112:115], v[242:249], v[204:211], v[112:115], v189, v189 op_sel_hi:[0,0,0]
	v_mfma_scale_f32_16x16x128_f8f6f4 v[104:107], v[234:241], v[226:233], v[104:107], v189, v189 op_sel_hi:[0,0,0]
	v_mfma_scale_f32_16x16x128_f8f6f4 v[96:99], v[242:249], v[226:233], v[96:99], v189, v189 op_sel_hi:[0,0,0]
	s_setprio 0
	s_mov_b32 m0, s81
	v_lshl_add_u64 v[186:187], v[186:187], 0, s[40:41]
	s_barrier
	ds_read_b128 v[16:19], v190 offset:49152
	ds_read_b128 v[24:27], v190 offset:51200
	ds_read_b128 v[20:23], v192 offset:49152
	ds_read_b128 v[28:31], v192 offset:51200
	ds_read_b128 v[176:179], v190 offset:53248
	ds_read_b128 v[204:207], v190 offset:55296
	ds_read_b128 v[180:183], v192 offset:53248
	ds_read_b128 v[208:211], v192 offset:55296
	global_load_lds_dwordx4 v[186:187], off
	v_lshl_add_u64 v[184:185], v[184:185], 0, s[40:41]
	s_mov_b32 m0, s82
	s_nop 0
	global_load_lds_dwordx4 v[184:185], off
	s_barrier
	s_waitcnt lgkmcnt(0)
	s_setprio 1
	v_mfma_scale_f32_16x16x128_f8f6f4 v[92:95], v[0:7], v[16:23], v[92:95], v189, v189 op_sel_hi:[0,0,0]
	v_mfma_scale_f32_16x16x128_f8f6f4 v[84:87], v[8:15], v[16:23], v[84:87], v189, v189 op_sel_hi:[0,0,0]
	v_mfma_scale_f32_16x16x128_f8f6f4 v[76:79], v[0:7], v[24:31], v[76:79], v189, v189 op_sel_hi:[0,0,0]
	v_mfma_scale_f32_16x16x128_f8f6f4 v[68:71], v[8:15], v[24:31], v[68:71], v189, v189 op_sel_hi:[0,0,0]
	v_mfma_scale_f32_16x16x128_f8f6f4 v[60:63], v[0:7], v[176:183], v[60:63], v189, v189 op_sel_hi:[0,0,0]
	v_mfma_scale_f32_16x16x128_f8f6f4 v[52:55], v[8:15], v[176:183], v[52:55], v189, v189 op_sel_hi:[0,0,0]
	v_mfma_scale_f32_16x16x128_f8f6f4 v[44:47], v[0:7], v[204:211], v[44:47], v189, v189 op_sel_hi:[0,0,0]
	v_mfma_scale_f32_16x16x128_f8f6f4 v[36:39], v[8:15], v[204:211], v[36:39], v189, v189 op_sel_hi:[0,0,0]
	s_setprio 0
	s_barrier
	s_add_u32 s24, s24, 0x20080
	s_addc_u32 s25, s25, 0
	s_mov_b32 m0, s83
	v_lshl_add_u64 v[0:1], s[24:25], 0, v[160:161]
	global_load_lds_dwordx4 v[0:1], off
	v_lshl_add_u64 v[0:1], s[24:25], 0, v[162:163]
	s_mov_b32 m0, s85
	s_nop 0
	global_load_lds_dwordx4 v[0:1], off
	s_waitcnt vmcnt(6)
	s_barrier
	s_setprio 1
	v_mfma_scale_f32_16x16x128_f8f6f4 v[88:91], v[234:241], v[16:23], v[88:91], v189, v189 op_sel_hi:[0,0,0]
	v_mfma_scale_f32_16x16x128_f8f6f4 v[80:83], v[242:249], v[16:23], v[80:83], v189, v189 op_sel_hi:[0,0,0]
	v_mfma_scale_f32_16x16x128_f8f6f4 v[72:75], v[234:241], v[24:31], v[72:75], v189, v189 op_sel_hi:[0,0,0]
	v_mfma_scale_f32_16x16x128_f8f6f4 v[64:67], v[242:249], v[24:31], v[64:67], v189, v189 op_sel_hi:[0,0,0]
	v_mfma_scale_f32_16x16x128_f8f6f4 v[56:59], v[234:241], v[176:183], v[56:59], v189, v189 op_sel_hi:[0,0,0]
	v_mfma_scale_f32_16x16x128_f8f6f4 v[48:51], v[242:249], v[176:183], v[48:51], v189, v189 op_sel_hi:[0,0,0]
	v_mfma_scale_f32_16x16x128_f8f6f4 v[40:43], v[234:241], v[204:211], v[40:43], v189, v189 op_sel_hi:[0,0,0]
	v_mfma_scale_f32_16x16x128_f8f6f4 v[32:35], v[242:249], v[204:211], v[32:35], v189, v189 op_sel_hi:[0,0,0]
	s_setprio 0
	s_add_i32 s64, s64, 2
	s_add_u32 s22, s22, 0x100
	s_addc_u32 s23, s23, 0
	s_add_u32 s2, s2, 0x100
	s_addc_u32 s3, s3, 0
	s_cmp_gt_u32 s64, 5
	s_barrier
	s_branch .LBB0_1556

.LBB0_1555:
	ds_read_b128 v[0:3], v191
	ds_read_b128 v[8:11], v191 offset:2048
	ds_read_b128 v[4:7], v193
	ds_read_b128 v[12:15], v193 offset:2048
	s_add_u32 s26, s22, 0x80
	s_addc_u32 s27, s23, 0
	s_and_b64 s[24:25], s[24:25], exec
	s_cselect_b32 s27, s19, s27
	s_cselect_b32 s26, s18, s26
	s_cselect_b32 s25, s17, s3
	s_cselect_b32 s24, s16, s2
	v_lshl_add_u64 v[16:17], s[22:23], 0, v[168:169]
	s_add_i32 m0, s44, 0xc000
	ds_read_b128 v[226:229], v190
	ds_read_b128 v[234:237], v190 offset:2048
	ds_read_b128 v[230:233], v192
	ds_read_b128 v[238:241], v192 offset:2048
	ds_read_b128 v[242:245], v190 offset:4096
	ds_read_b128 v[204:207], v190 offset:6144
	ds_read_b128 v[246:249], v192 offset:4096
	ds_read_b128 v[208:211], v192 offset:6144
	global_load_lds_dwordx4 v[16:17], off
	v_lshl_add_u64 v[16:17], s[22:23], 0, v[174:175]
	s_add_i32 m0, s44, 0xe000
	s_nop 0
	global_load_lds_dwordx4 v[16:17], off
	s_waitcnt lgkmcnt(8)
	s_barrier
	s_waitcnt lgkmcnt(0)
	s_setprio 1
	v_mfma_scale_f32_16x16x128_f8f6f4 v[156:159], v[0:7], v[226:233], v[156:159], v189, v189 op_sel_hi:[0,0,0]
	v_mfma_scale_f32_16x16x128_f8f6f4 v[148:151], v[8:15], v[226:233], v[148:151], v189, v189 op_sel_hi:[0,0,0]
	v_mfma_scale_f32_16x16x128_f8f6f4 v[140:143], v[0:7], v[234:241], v[140:143], v189, v189 op_sel_hi:[0,0,0]
	v_mfma_scale_f32_16x16x128_f8f6f4 v[132:135], v[8:15], v[234:241], v[132:135], v189, v189 op_sel_hi:[0,0,0]
	v_mfma_scale_f32_16x16x128_f8f6f4 v[124:127], v[0:7], v[242:249], v[124:127], v189, v189 op_sel_hi:[0,0,0]
	v_mfma_scale_f32_16x16x128_f8f6f4 v[116:119], v[8:15], v[242:249], v[116:119], v189, v189 op_sel_hi:[0,0,0]
	v_mfma_scale_f32_16x16x128_f8f6f4 v[108:111], v[0:7], v[204:211], v[108:111], v189, v189 op_sel_hi:[0,0,0]
	v_mfma_scale_f32_16x16x128_f8f6f4 v[100:103], v[8:15], v[204:211], v[100:103], v189, v189 op_sel_hi:[0,0,0]
	s_setprio 0
	s_barrier
	s_mov_b32 m0, s46
	v_lshl_add_u64 v[180:181], s[24:25], 0, v[160:161]
	ds_read_b128 v[16:19], v191 offset:16384
	ds_read_b128 v[24:27], v191 offset:18432
	ds_read_b128 v[20:23], v193 offset:16384
	ds_read_b128 v[28:31], v193 offset:18432
	global_load_lds_dwordx4 v[180:181], off
	v_lshl_add_u64 v[182:183], s[24:25], 0, v[162:163]
	s_mov_b32 m0, s47
	s_nop 0
	global_load_lds_dwordx4 v[182:183], off
	s_barrier
	s_waitcnt lgkmcnt(0)
	s_setprio 1
	v_mfma_scale_f32_16x16x128_f8f6f4 v[152:155], v[16:23], v[226:233], v[152:155], v189, v189 op_sel_hi:[0,0,0]
	v_mfma_scale_f32_16x16x128_f8f6f4 v[144:147], v[24:31], v[226:233], v[144:147], v189, v189 op_sel_hi:[0,0,0]
	v_mfma_scale_f32_16x16x128_f8f6f4 v[136:139], v[16:23], v[234:241], v[136:139], v189, v189 op_sel_hi:[0,0,0]
	v_mfma_scale_f32_16x16x128_f8f6f4 v[128:131], v[24:31], v[234:241], v[128:131], v189, v189 op_sel_hi:[0,0,0]
	v_mfma_scale_f32_16x16x128_f8f6f4 v[120:123], v[16:23], v[242:249], v[120:123], v189, v189 op_sel_hi:[0,0,0]
	v_mfma_scale_f32_16x16x128_f8f6f4 v[112:115], v[24:31], v[242:249], v[112:115], v189, v189 op_sel_hi:[0,0,0]
	v_mfma_scale_f32_16x16x128_f8f6f4 v[104:107], v[16:23], v[204:211], v[104:107], v189, v189 op_sel_hi:[0,0,0]
	v_mfma_scale_f32_16x16x128_f8f6f4 v[96:99], v[24:31], v[204:211], v[96:99], v189, v189 op_sel_hi:[0,0,0]
	s_setprio 0
	s_mov_b32 m0, s44
	s_barrier
	ds_read_b128 v[204:207], v190 offset:16384
	ds_read_b128 v[226:229], v190 offset:18432
	ds_read_b128 v[208:211], v192 offset:16384
	ds_read_b128 v[230:233], v192 offset:18432
	ds_read_b128 v[234:237], v190 offset:20480
	ds_read_b128 v[242:245], v190 offset:22528
	ds_read_b128 v[238:241], v192 offset:20480
	ds_read_b128 v[246:249], v192 offset:22528
	global_load_lds_dwordx4 v186, s[26:27]
	s_mov_b32 m0, s50
	v_mov_b32_e32 v187, v173
	global_load_lds_dwordx4 v184, s[26:27]
	s_barrier
	s_waitcnt lgkmcnt(0)
	v_mov_b32_e32 v185, v173
	v_lshl_add_u64 v[186:187], s[26:27], 0, v[186:187]
	v_lshl_add_u64 v[184:185], s[26:27], 0, v[184:185]
	s_setprio 1
	s_waitcnt lgkmcnt(0)
	v_mfma_scale_f32_16x16x128_f8f6f4 v[92:95], v[0:7], v[204:211], v[92:95], v189, v189 op_sel_hi:[0,0,0]
	v_mfma_scale_f32_16x16x128_f8f6f4 v[84:87], v[8:15], v[204:211], v[84:87], v189, v189 op_sel_hi:[0,0,0]
	v_mfma_scale_f32_16x16x128_f8f6f4 v[76:79], v[0:7], v[226:233], v[76:79], v189, v189 op_sel_hi:[0,0,0]
	v_mfma_scale_f32_16x16x128_f8f6f4 v[68:71], v[8:15], v[226:233], v[68:71], v189, v189 op_sel_hi:[0,0,0]
	v_mfma_scale_f32_16x16x128_f8f6f4 v[60:63], v[0:7], v[234:241], v[60:63], v189, v189 op_sel_hi:[0,0,0]
	v_mfma_scale_f32_16x16x128_f8f6f4 v[52:55], v[8:15], v[234:241], v[52:55], v189, v189 op_sel_hi:[0,0,0]
	v_mfma_scale_f32_16x16x128_f8f6f4 v[44:47], v[0:7], v[242:249], v[44:47], v189, v189 op_sel_hi:[0,0,0]
	v_mfma_scale_f32_16x16x128_f8f6f4 v[36:39], v[8:15], v[242:249], v[36:39], v189, v189 op_sel_hi:[0,0,0]
	s_setprio 0
	s_barrier
	s_add_u32 s72, s24, 0x20000
	s_addc_u32 s73, s25, 0
	s_mov_b32 m0, s51
	v_lshl_add_u64 v[0:1], s[72:73], 0, v[160:161]
	global_load_lds_dwordx4 v[0:1], off
	v_lshl_add_u64 v[0:1], s[72:73], 0, v[162:163]
	s_mov_b32 m0, s56
	s_nop 0
	global_load_lds_dwordx4 v[0:1], off
	s_waitcnt vmcnt(6)
	s_barrier
	s_setprio 1
	v_mfma_scale_f32_16x16x128_f8f6f4 v[88:91], v[16:23], v[204:211], v[88:91], v189, v189 op_sel_hi:[0,0,0]
	v_mfma_scale_f32_16x16x128_f8f6f4 v[80:83], v[24:31], v[204:211], v[80:83], v189, v189 op_sel_hi:[0,0,0]
	v_mfma_scale_f32_16x16x128_f8f6f4 v[72:75], v[16:23], v[226:233], v[72:75], v189, v189 op_sel_hi:[0,0,0]
	v_mfma_scale_f32_16x16x128_f8f6f4 v[64:67], v[24:31], v[226:233], v[64:67], v189, v189 op_sel_hi:[0,0,0]
	v_mfma_scale_f32_16x16x128_f8f6f4 v[56:59], v[16:23], v[234:241], v[56:59], v189, v189 op_sel_hi:[0,0,0]
	v_mfma_scale_f32_16x16x128_f8f6f4 v[48:51], v[24:31], v[234:241], v[48:51], v189, v189 op_sel_hi:[0,0,0]
	v_mfma_scale_f32_16x16x128_f8f6f4 v[40:43], v[16:23], v[242:249], v[40:43], v189, v189 op_sel_hi:[0,0,0]
	v_mfma_scale_f32_16x16x128_f8f6f4 v[32:35], v[24:31], v[242:249], v[32:35], v189, v189 op_sel_hi:[0,0,0]
	s_setprio 0
	s_barrier
	ds_read_b128 v[0:3], v191 offset:32768
	ds_read_b128 v[8:11], v191 offset:34816
	ds_read_b128 v[4:7], v193 offset:32768
	ds_read_b128 v[12:15], v193 offset:34816
	s_mov_b32 m0, s65
	v_lshl_add_u64 v[178:179], s[26:27], 0, v[178:179]
	ds_read_b128 v[16:19], v190 offset:32768
	ds_read_b128 v[24:27], v190 offset:34816
	ds_read_b128 v[20:23], v192 offset:32768
	ds_read_b128 v[28:31], v192 offset:34816
	ds_read_b128 v[204:207], v190 offset:36864
	ds_read_b128 v[226:229], v190 offset:38912
	ds_read_b128 v[208:211], v192 offset:36864
	ds_read_b128 v[230:233], v192 offset:38912
	global_load_lds_dwordx4 v[178:179], off
	v_lshl_add_u64 v[176:177], s[26:27], 0, v[176:177]
	s_mov_b32 m0, s70
	s_nop 0
	global_load_lds_dwordx4 v[176:177], off
	s_waitcnt lgkmcnt(8)
	s_barrier
	s_waitcnt lgkmcnt(0)
	s_setprio 1
	v_mfma_scale_f32_16x16x128_f8f6f4 v[156:159], v[0:7], v[16:23], v[156:159], v189, v189 op_sel_hi:[0,0,0]
	v_mfma_scale_f32_16x16x128_f8f6f4 v[148:151], v[8:15], v[16:23], v[148:151], v189, v189 op_sel_hi:[0,0,0]
	v_mfma_scale_f32_16x16x128_f8f6f4 v[140:143], v[0:7], v[24:31], v[140:143], v189, v189 op_sel_hi:[0,0,0]
	v_mfma_scale_f32_16x16x128_f8f6f4 v[132:135], v[8:15], v[24:31], v[132:135], v189, v189 op_sel_hi:[0,0,0]
	v_mfma_scale_f32_16x16x128_f8f6f4 v[124:127], v[0:7], v[204:211], v[124:127], v189, v189 op_sel_hi:[0,0,0]
	v_mfma_scale_f32_16x16x128_f8f6f4 v[116:119], v[8:15], v[204:211], v[116:119], v189, v189 op_sel_hi:[0,0,0]
	v_mfma_scale_f32_16x16x128_f8f6f4 v[108:111], v[0:7], v[226:233], v[108:111], v189, v189 op_sel_hi:[0,0,0]
	v_mfma_scale_f32_16x16x128_f8f6f4 v[100:103], v[8:15], v[226:233], v[100:103], v189, v189 op_sel_hi:[0,0,0]
	s_setprio 0
	s_barrier
	s_mov_b32 m0, s71
	v_lshl_add_u64 v[176:177], v[180:181], 0, s[40:41]
	ds_read_b128 v[234:237], v191 offset:49152
	ds_read_b128 v[242:245], v191 offset:51200
	ds_read_b128 v[238:241], v193 offset:49152
	ds_read_b128 v[246:249], v193 offset:51200
	global_load_lds_dwordx4 v[176:177], off
	v_lshl_add_u64 v[176:177], v[182:183], 0, s[40:41]
	s_mov_b32 m0, s80
	s_nop 0
	global_load_lds_dwordx4 v[176:177], off
	s_barrier
	s_waitcnt lgkmcnt(0)
	s_setprio 1
	v_mfma_scale_f32_16x16x128_f8f6f4 v[152:155], v[234:241], v[16:23], v[152:155], v189, v189 op_sel_hi:[0,0,0]
	v_mfma_scale_f32_16x16x128_f8f6f4 v[144:147], v[242:249], v[16:23], v[144:147], v189, v189 op_sel_hi:[0,0,0]
	v_mfma_scale_f32_16x16x128_f8f6f4 v[136:139], v[234:241], v[24:31], v[136:139], v189, v189 op_sel_hi:[0,0,0]
	v_mfma_scale_f32_16x16x128_f8f6f4 v[128:131], v[242:249], v[24:31], v[128:131], v189, v189 op_sel_hi:[0,0,0]
	v_mfma_scale_f32_16x16x128_f8f6f4 v[120:123], v[234:241], v[204:211], v[120:123], v189, v189 op_sel_hi:[0,0,0]
	v_mfma_scale_f32_16x16x128_f8f6f4 v[112:115], v[242:249], v[204:211], v[112:115], v189, v189 op_sel_hi:[0,0,0]
	v_mfma_scale_f32_16x16x128_f8f6f4 v[104:107], v[234:241], v[226:233], v[104:107], v189, v189 op_sel_hi:[0,0,0]
	v_mfma_scale_f32_16x16x128_f8f6f4 v[96:99], v[242:249], v[226:233], v[96:99], v189, v189 op_sel_hi:[0,0,0]
	s_setprio 0
	s_mov_b32 m0, s81
	v_lshl_add_u64 v[186:187], v[186:187], 0, s[40:41]
	s_barrier
	ds_read_b128 v[16:19], v190 offset:49152
	ds_read_b128 v[24:27], v190 offset:51200
	ds_read_b128 v[20:23], v192 offset:49152
	ds_read_b128 v[28:31], v192 offset:51200
	ds_read_b128 v[176:179], v190 offset:53248
	ds_read_b128 v[204:207], v190 offset:55296
	ds_read_b128 v[180:183], v192 offset:53248
	ds_read_b128 v[208:211], v192 offset:55296
	global_load_lds_dwordx4 v[186:187], off
	v_lshl_add_u64 v[184:185], v[184:185], 0, s[40:41]
	s_mov_b32 m0, s82
	s_nop 0
	global_load_lds_dwordx4 v[184:185], off
	s_barrier
	s_waitcnt lgkmcnt(0)
	s_setprio 1
	v_mfma_scale_f32_16x16x128_f8f6f4 v[92:95], v[0:7], v[16:23], v[92:95], v189, v189 op_sel_hi:[0,0,0]
	v_mfma_scale_f32_16x16x128_f8f6f4 v[84:87], v[8:15], v[16:23], v[84:87], v189, v189 op_sel_hi:[0,0,0]
	v_mfma_scale_f32_16x16x128_f8f6f4 v[76:79], v[0:7], v[24:31], v[76:79], v189, v189 op_sel_hi:[0,0,0]
	v_mfma_scale_f32_16x16x128_f8f6f4 v[68:71], v[8:15], v[24:31], v[68:71], v189, v189 op_sel_hi:[0,0,0]
	v_mfma_scale_f32_16x16x128_f8f6f4 v[60:63], v[0:7], v[176:183], v[60:63], v189, v189 op_sel_hi:[0,0,0]
	v_mfma_scale_f32_16x16x128_f8f6f4 v[52:55], v[8:15], v[176:183], v[52:55], v189, v189 op_sel_hi:[0,0,0]
	v_mfma_scale_f32_16x16x128_f8f6f4 v[44:47], v[0:7], v[204:211], v[44:47], v189, v189 op_sel_hi:[0,0,0]
	v_mfma_scale_f32_16x16x128_f8f6f4 v[36:39], v[8:15], v[204:211], v[36:39], v189, v189 op_sel_hi:[0,0,0]
	s_setprio 0
	s_barrier
	s_add_u32 s24, s24, 0x20080
	s_addc_u32 s25, s25, 0
	s_mov_b32 m0, s83
	v_lshl_add_u64 v[0:1], s[24:25], 0, v[160:161]
	global_load_lds_dwordx4 v[0:1], off
	v_lshl_add_u64 v[0:1], s[24:25], 0, v[162:163]
	s_mov_b32 m0, s85
	s_nop 0
	global_load_lds_dwordx4 v[0:1], off
	s_waitcnt vmcnt(6)
	s_barrier
	s_setprio 1
	v_mfma_scale_f32_16x16x128_f8f6f4 v[88:91], v[234:241], v[16:23], v[88:91], v189, v189 op_sel_hi:[0,0,0]
	v_mfma_scale_f32_16x16x128_f8f6f4 v[80:83], v[242:249], v[16:23], v[80:83], v189, v189 op_sel_hi:[0,0,0]
	v_mfma_scale_f32_16x16x128_f8f6f4 v[72:75], v[234:241], v[24:31], v[72:75], v189, v189 op_sel_hi:[0,0,0]
	v_mfma_scale_f32_16x16x128_f8f6f4 v[64:67], v[242:249], v[24:31], v[64:67], v189, v189 op_sel_hi:[0,0,0]
	v_mfma_scale_f32_16x16x128_f8f6f4 v[56:59], v[234:241], v[176:183], v[56:59], v189, v189 op_sel_hi:[0,0,0]
	v_mfma_scale_f32_16x16x128_f8f6f4 v[48:51], v[242:249], v[176:183], v[48:51], v189, v189 op_sel_hi:[0,0,0]
	v_mfma_scale_f32_16x16x128_f8f6f4 v[40:43], v[234:241], v[204:211], v[40:43], v189, v189 op_sel_hi:[0,0,0]
	v_mfma_scale_f32_16x16x128_f8f6f4 v[32:35], v[242:249], v[204:211], v[32:35], v189, v189 op_sel_hi:[0,0,0]
	s_setprio 0
	s_add_i32 s64, s64, 2
	s_add_u32 s22, s22, 0x100
	s_addc_u32 s23, s23, 0
	s_add_u32 s2, s2, 0x100
	s_addc_u32 s3, s3, 0
	s_cmp_gt_u32 s64, 5
	s_barrier
	s_cbranch_scc1 .LBB0_1540

.Lpeel_dn:
	s_mov_b64 s[24:25], 0
	v_mov_b64_e32 v[176:177], v[170:171]
	v_mov_b64_e32 v[178:179], v[166:167]
	v_mov_b32_e32 v184, v174
	v_mov_b32_e32 v172, v168
	ds_read_b128 v[0:3], v190
	ds_read_b128 v[8:11], v190 offset:2048
	ds_read_b128 v[4:7], v192
	ds_read_b128 v[12:15], v192 offset:2048
	s_add_u32 s26, s22, 0x80
	s_addc_u32 s27, s23, 0
	s_and_b64 s[24:25], s[24:25], exec
	s_cselect_b32 s27, s19, s27
	s_cselect_b32 s26, s18, s26
	s_cselect_b32 s25, s17, s83
	s_cselect_b32 s24, s16, s7
	v_lshl_add_u64 v[16:17], s[22:23], 0, v[166:167]
	s_add_i32 m0, s13, 0xc000
	ds_read_b128 v[204:207], v189
	ds_read_b128 v[216:219], v189 offset:2048
	ds_read_b128 v[208:211], v191
	ds_read_b128 v[220:223], v191 offset:2048
	ds_read_b128 v[224:227], v189 offset:4096
	ds_read_b128 v[232:235], v189 offset:6144
	ds_read_b128 v[228:231], v191 offset:4096
	ds_read_b128 v[236:239], v191 offset:6144
	global_load_lds_dwordx4 v[16:17], off
	v_lshl_add_u64 v[16:17], s[22:23], 0, v[170:171]
	s_add_i32 m0, s13, 0xe000
	s_nop 0
	global_load_lds_dwordx4 v[16:17], off
	s_waitcnt lgkmcnt(8)
	s_barrier
	s_waitcnt lgkmcnt(0)
	s_setprio 1
	v_mfma_scale_f32_16x16x128_f8f6f4 v[156:159], v[0:7], v[204:211], 0, v188, v188 op_sel_hi:[0,0,0]
	v_mfma_scale_f32_16x16x128_f8f6f4 v[152:155], v[8:15], v[204:211], 0, v188, v188 op_sel_hi:[0,0,0]
	v_mfma_scale_f32_16x16x128_f8f6f4 v[148:151], v[0:7], v[216:223], 0, v188, v188 op_sel_hi:[0,0,0]
	v_mfma_scale_f32_16x16x128_f8f6f4 v[144:147], v[8:15], v[216:223], 0, v188, v188 op_sel_hi:[0,0,0]
	v_mfma_scale_f32_16x16x128_f8f6f4 v[140:143], v[0:7], v[224:231], 0, v188, v188 op_sel_hi:[0,0,0]
	v_mfma_scale_f32_16x16x128_f8f6f4 v[136:139], v[8:15], v[224:231], 0, v188, v188 op_sel_hi:[0,0,0]
	v_mfma_scale_f32_16x16x128_f8f6f4 v[132:135], v[0:7], v[232:239], 0, v188, v188 op_sel_hi:[0,0,0]
	v_mfma_scale_f32_16x16x128_f8f6f4 v[128:131], v[8:15], v[232:239], 0, v188, v188 op_sel_hi:[0,0,0]
	s_setprio 0
	s_barrier
	s_mov_b32 m0, s15
	v_lshl_add_u64 v[180:181], s[24:25], 0, v[162:163]
	ds_read_b128 v[16:19], v190 offset:16384
	ds_read_b128 v[24:27], v190 offset:18432
	ds_read_b128 v[20:23], v192 offset:16384
	ds_read_b128 v[28:31], v192 offset:18432
	global_load_lds_dwordx4 v[180:181], off
	v_lshl_add_u64 v[182:183], s[24:25], 0, v[164:165]
	s_mov_b32 m0, s31
	s_nop 0
	global_load_lds_dwordx4 v[182:183], off
	s_barrier
	s_waitcnt lgkmcnt(0)
	s_setprio 1
	v_mfma_scale_f32_16x16x128_f8f6f4 v[100:103], v[16:23], v[204:211], 0, v188, v188 op_sel_hi:[0,0,0]
	v_mfma_scale_f32_16x16x128_f8f6f4 v[96:99], v[24:31], v[204:211], 0, v188, v188 op_sel_hi:[0,0,0]
	v_mfma_scale_f32_16x16x128_f8f6f4 v[84:87], v[16:23], v[216:223], 0, v188, v188 op_sel_hi:[0,0,0]
	v_mfma_scale_f32_16x16x128_f8f6f4 v[80:83], v[24:31], v[216:223], 0, v188, v188 op_sel_hi:[0,0,0]
	v_mfma_scale_f32_16x16x128_f8f6f4 v[76:79], v[16:23], v[224:231], 0, v188, v188 op_sel_hi:[0,0,0]
	v_mfma_scale_f32_16x16x128_f8f6f4 v[72:75], v[24:31], v[224:231], 0, v188, v188 op_sel_hi:[0,0,0]
	v_mfma_scale_f32_16x16x128_f8f6f4 v[68:71], v[16:23], v[232:239], 0, v188, v188 op_sel_hi:[0,0,0]
	v_mfma_scale_f32_16x16x128_f8f6f4 v[64:67], v[24:31], v[232:239], 0, v188, v188 op_sel_hi:[0,0,0]
	s_setprio 0
	s_mov_b32 m0, s13
	s_barrier
	ds_read_b128 v[204:207], v189 offset:16384
	ds_read_b128 v[216:219], v189 offset:18432
	ds_read_b128 v[208:211], v191 offset:16384
	ds_read_b128 v[220:223], v191 offset:18432
	ds_read_b128 v[224:227], v189 offset:20480
	ds_read_b128 v[232:235], v189 offset:22528
	ds_read_b128 v[228:231], v191 offset:20480
	ds_read_b128 v[236:239], v191 offset:22528
	global_load_lds_dwordx4 v172, s[26:27]
	s_mov_b32 m0, s44
	v_mov_b32_e32 v185, v173
	global_load_lds_dwordx4 v184, s[26:27]
	s_barrier
	s_waitcnt lgkmcnt(0)
	v_lshl_add_u64 v[186:187], s[26:27], 0, v[172:173]
	v_lshl_add_u64 v[184:185], s[26:27], 0, v[184:185]
	s_setprio 1
	s_waitcnt lgkmcnt(0)
	v_mfma_scale_f32_16x16x128_f8f6f4 v[124:127], v[0:7], v[204:211], 0, v188, v188 op_sel_hi:[0,0,0]
	v_mfma_scale_f32_16x16x128_f8f6f4 v[120:123], v[8:15], v[204:211], 0, v188, v188 op_sel_hi:[0,0,0]
	v_mfma_scale_f32_16x16x128_f8f6f4 v[116:119], v[0:7], v[216:223], 0, v188, v188 op_sel_hi:[0,0,0]
	v_mfma_scale_f32_16x16x128_f8f6f4 v[112:115], v[8:15], v[216:223], 0, v188, v188 op_sel_hi:[0,0,0]
	v_mfma_scale_f32_16x16x128_f8f6f4 v[108:111], v[0:7], v[224:231], 0, v188, v188 op_sel_hi:[0,0,0]
	v_mfma_scale_f32_16x16x128_f8f6f4 v[104:107], v[8:15], v[224:231], 0, v188, v188 op_sel_hi:[0,0,0]
	v_mfma_scale_f32_16x16x128_f8f6f4 v[92:95], v[0:7], v[232:239], 0, v188, v188 op_sel_hi:[0,0,0]
	v_mfma_scale_f32_16x16x128_f8f6f4 v[88:91], v[8:15], v[232:239], 0, v188, v188 op_sel_hi:[0,0,0]
	s_setprio 0
	s_barrier
	s_add_u32 s90, s24, 0x20000
	s_addc_u32 s91, s25, 0
	s_mov_b32 m0, s46
	v_lshl_add_u64 v[0:1], s[90:91], 0, v[162:163]
	global_load_lds_dwordx4 v[0:1], off
	v_lshl_add_u64 v[0:1], s[90:91], 0, v[164:165]
	s_mov_b32 m0, s47
	s_nop 0
	global_load_lds_dwordx4 v[0:1], off
	s_waitcnt vmcnt(6)
	s_barrier
	s_setprio 1
	v_mfma_scale_f32_16x16x128_f8f6f4 v[60:63], v[16:23], v[204:211], 0, v188, v188 op_sel_hi:[0,0,0]
	v_mfma_scale_f32_16x16x128_f8f6f4 v[56:59], v[24:31], v[204:211], 0, v188, v188 op_sel_hi:[0,0,0]
	v_mfma_scale_f32_16x16x128_f8f6f4 v[52:55], v[16:23], v[216:223], 0, v188, v188 op_sel_hi:[0,0,0]
	v_mfma_scale_f32_16x16x128_f8f6f4 v[48:51], v[24:31], v[216:223], 0, v188, v188 op_sel_hi:[0,0,0]
	v_mfma_scale_f32_16x16x128_f8f6f4 v[44:47], v[16:23], v[224:231], 0, v188, v188 op_sel_hi:[0,0,0]
	v_mfma_scale_f32_16x16x128_f8f6f4 v[40:43], v[24:31], v[224:231], 0, v188, v188 op_sel_hi:[0,0,0]
	v_mfma_scale_f32_16x16x128_f8f6f4 v[36:39], v[16:23], v[232:239], 0, v188, v188 op_sel_hi:[0,0,0]
	v_mfma_scale_f32_16x16x128_f8f6f4 v[32:35], v[24:31], v[232:239], 0, v188, v188 op_sel_hi:[0,0,0]
	s_setprio 0
	s_barrier
	ds_read_b128 v[0:3], v190 offset:32768
	ds_read_b128 v[8:11], v190 offset:34816
	ds_read_b128 v[4:7], v192 offset:32768
	ds_read_b128 v[12:15], v192 offset:34816
	s_mov_b32 m0, s50
	v_lshl_add_u64 v[178:179], s[26:27], 0, v[178:179]
	ds_read_b128 v[16:19], v189 offset:32768
	ds_read_b128 v[24:27], v189 offset:34816
	ds_read_b128 v[20:23], v191 offset:32768
	ds_read_b128 v[28:31], v191 offset:34816
	ds_read_b128 v[204:207], v189 offset:36864
	ds_read_b128 v[216:219], v189 offset:38912
	ds_read_b128 v[208:211], v191 offset:36864
	ds_read_b128 v[220:223], v191 offset:38912
	global_load_lds_dwordx4 v[178:179], off
	v_lshl_add_u64 v[176:177], s[26:27], 0, v[176:177]
	s_mov_b32 m0, s51
	s_nop 0
	global_load_lds_dwordx4 v[176:177], off
	s_waitcnt lgkmcnt(8)
	s_barrier
	s_waitcnt lgkmcnt(0)
	s_setprio 1
	v_mfma_scale_f32_16x16x128_f8f6f4 v[156:159], v[0:7], v[16:23], v[156:159], v188, v188 op_sel_hi:[0,0,0]
	v_mfma_scale_f32_16x16x128_f8f6f4 v[152:155], v[8:15], v[16:23], v[152:155], v188, v188 op_sel_hi:[0,0,0]
	v_mfma_scale_f32_16x16x128_f8f6f4 v[148:151], v[0:7], v[24:31], v[148:151], v188, v188 op_sel_hi:[0,0,0]
	v_mfma_scale_f32_16x16x128_f8f6f4 v[144:147], v[8:15], v[24:31], v[144:147], v188, v188 op_sel_hi:[0,0,0]
	v_mfma_scale_f32_16x16x128_f8f6f4 v[140:143], v[0:7], v[204:211], v[140:143], v188, v188 op_sel_hi:[0,0,0]
	v_mfma_scale_f32_16x16x128_f8f6f4 v[136:139], v[8:15], v[204:211], v[136:139], v188, v188 op_sel_hi:[0,0,0]
	v_mfma_scale_f32_16x16x128_f8f6f4 v[132:135], v[0:7], v[216:223], v[132:135], v188, v188 op_sel_hi:[0,0,0]
	v_mfma_scale_f32_16x16x128_f8f6f4 v[128:131], v[8:15], v[216:223], v[128:131], v188, v188 op_sel_hi:[0,0,0]
	s_setprio 0
	s_barrier
	s_mov_b32 m0, s56
	v_lshl_add_u64 v[176:177], v[180:181], 0, s[40:41]
	ds_read_b128 v[224:227], v190 offset:49152
	ds_read_b128 v[232:235], v190 offset:51200
	ds_read_b128 v[228:231], v192 offset:49152
	ds_read_b128 v[236:239], v192 offset:51200
	global_load_lds_dwordx4 v[176:177], off
	v_lshl_add_u64 v[176:177], v[182:183], 0, s[40:41]
	s_mov_b32 m0, s57
	s_nop 0
	global_load_lds_dwordx4 v[176:177], off
	s_barrier
	s_waitcnt lgkmcnt(0)
	s_setprio 1
	v_mfma_scale_f32_16x16x128_f8f6f4 v[100:103], v[224:231], v[16:23], v[100:103], v188, v188 op_sel_hi:[0,0,0]
	v_mfma_scale_f32_16x16x128_f8f6f4 v[96:99], v[232:239], v[16:23], v[96:99], v188, v188 op_sel_hi:[0,0,0]
	v_mfma_scale_f32_16x16x128_f8f6f4 v[84:87], v[224:231], v[24:31], v[84:87], v188, v188 op_sel_hi:[0,0,0]
	v_mfma_scale_f32_16x16x128_f8f6f4 v[80:83], v[232:239], v[24:31], v[80:83], v188, v188 op_sel_hi:[0,0,0]
	v_mfma_scale_f32_16x16x128_f8f6f4 v[76:79], v[224:231], v[204:211], v[76:79], v188, v188 op_sel_hi:[0,0,0]
	v_mfma_scale_f32_16x16x128_f8f6f4 v[72:75], v[232:239], v[204:211], v[72:75], v188, v188 op_sel_hi:[0,0,0]
	v_mfma_scale_f32_16x16x128_f8f6f4 v[68:71], v[224:231], v[216:223], v[68:71], v188, v188 op_sel_hi:[0,0,0]
	v_mfma_scale_f32_16x16x128_f8f6f4 v[64:67], v[232:239], v[216:223], v[64:67], v188, v188 op_sel_hi:[0,0,0]
	s_setprio 0
	s_mov_b32 m0, s64
	v_lshl_add_u64 v[186:187], v[186:187], 0, s[40:41]
	s_barrier
	ds_read_b128 v[16:19], v189 offset:49152
	ds_read_b128 v[24:27], v189 offset:51200
	ds_read_b128 v[20:23], v191 offset:49152
	ds_read_b128 v[28:31], v191 offset:51200
	ds_read_b128 v[176:179], v189 offset:53248
	ds_read_b128 v[204:207], v189 offset:55296
	ds_read_b128 v[180:183], v191 offset:53248
	ds_read_b128 v[208:211], v191 offset:55296
	global_load_lds_dwordx4 v[186:187], off
	v_lshl_add_u64 v[184:185], v[184:185], 0, s[40:41]
	s_mov_b32 m0, s65
	s_nop 0
	global_load_lds_dwordx4 v[184:185], off
	s_barrier
	s_waitcnt lgkmcnt(0)
	s_setprio 1
	v_mfma_scale_f32_16x16x128_f8f6f4 v[124:127], v[0:7], v[16:23], v[124:127], v188, v188 op_sel_hi:[0,0,0]
	v_mfma_scale_f32_16x16x128_f8f6f4 v[120:123], v[8:15], v[16:23], v[120:123], v188, v188 op_sel_hi:[0,0,0]
	v_mfma_scale_f32_16x16x128_f8f6f4 v[116:119], v[0:7], v[24:31], v[116:119], v188, v188 op_sel_hi:[0,0,0]
	v_mfma_scale_f32_16x16x128_f8f6f4 v[112:115], v[8:15], v[24:31], v[112:115], v188, v188 op_sel_hi:[0,0,0]
	v_mfma_scale_f32_16x16x128_f8f6f4 v[108:111], v[0:7], v[176:183], v[108:111], v188, v188 op_sel_hi:[0,0,0]
	v_mfma_scale_f32_16x16x128_f8f6f4 v[104:107], v[8:15], v[176:183], v[104:107], v188, v188 op_sel_hi:[0,0,0]
	v_mfma_scale_f32_16x16x128_f8f6f4 v[92:95], v[0:7], v[204:211], v[92:95], v188, v188 op_sel_hi:[0,0,0]
	v_mfma_scale_f32_16x16x128_f8f6f4 v[88:91], v[8:15], v[204:211], v[88:91], v188, v188 op_sel_hi:[0,0,0]
	s_setprio 0
	s_barrier
	s_add_u32 s24, s24, 0x20080
	s_addc_u32 s25, s25, 0
	s_mov_b32 m0, s70
	v_lshl_add_u64 v[0:1], s[24:25], 0, v[162:163]
	global_load_lds_dwordx4 v[0:1], off
	v_lshl_add_u64 v[0:1], s[24:25], 0, v[164:165]
	s_mov_b32 m0, s71
	s_nop 0
	global_load_lds_dwordx4 v[0:1], off
	s_waitcnt vmcnt(6)
	s_barrier
	s_setprio 1
	v_mfma_scale_f32_16x16x128_f8f6f4 v[60:63], v[224:231], v[16:23], v[60:63], v188, v188 op_sel_hi:[0,0,0]
	v_mfma_scale_f32_16x16x128_f8f6f4 v[56:59], v[232:239], v[16:23], v[56:59], v188, v188 op_sel_hi:[0,0,0]
	v_mfma_scale_f32_16x16x128_f8f6f4 v[52:55], v[224:231], v[24:31], v[52:55], v188, v188 op_sel_hi:[0,0,0]
	v_mfma_scale_f32_16x16x128_f8f6f4 v[48:51], v[232:239], v[24:31], v[48:51], v188, v188 op_sel_hi:[0,0,0]
	v_mfma_scale_f32_16x16x128_f8f6f4 v[44:47], v[224:231], v[176:183], v[44:47], v188, v188 op_sel_hi:[0,0,0]
	v_mfma_scale_f32_16x16x128_f8f6f4 v[40:43], v[232:239], v[176:183], v[40:43], v188, v188 op_sel_hi:[0,0,0]
	v_mfma_scale_f32_16x16x128_f8f6f4 v[36:39], v[224:231], v[204:211], v[36:39], v188, v188 op_sel_hi:[0,0,0]
	v_mfma_scale_f32_16x16x128_f8f6f4 v[32:35], v[232:239], v[204:211], v[32:35], v188, v188 op_sel_hi:[0,0,0]
	s_setprio 0
	s_add_i32 s85, s85, 2
	s_add_u32 s22, s22, 0x100
	s_addc_u32 s23, s23, 0
	s_add_u32 s7, s7, 0x100
	s_addc_u32 s83, s83, 0
	s_cmp_gt_u32 s85, 5
	s_barrier
	s_branch .LBB0_1667
.LBB0_1666:
	ds_read_b128 v[0:3], v190
	ds_read_b128 v[8:11], v190 offset:2048
	ds_read_b128 v[4:7], v192
	ds_read_b128 v[12:15], v192 offset:2048
	s_add_u32 s26, s22, 0x80
	s_addc_u32 s27, s23, 0
	s_and_b64 s[24:25], s[24:25], exec
	s_cselect_b32 s27, s19, s27
	s_cselect_b32 s26, s18, s26
	s_cselect_b32 s25, s17, s83
	s_cselect_b32 s24, s16, s7
	v_lshl_add_u64 v[16:17], s[22:23], 0, v[166:167]
	s_add_i32 m0, s13, 0xc000
	ds_read_b128 v[204:207], v189
	ds_read_b128 v[216:219], v189 offset:2048
	ds_read_b128 v[208:211], v191
	ds_read_b128 v[220:223], v191 offset:2048
	ds_read_b128 v[224:227], v189 offset:4096
	ds_read_b128 v[232:235], v189 offset:6144
	ds_read_b128 v[228:231], v191 offset:4096
	ds_read_b128 v[236:239], v191 offset:6144
	global_load_lds_dwordx4 v[16:17], off
	v_lshl_add_u64 v[16:17], s[22:23], 0, v[170:171]
	s_add_i32 m0, s13, 0xe000
	s_nop 0
	global_load_lds_dwordx4 v[16:17], off
	s_waitcnt lgkmcnt(8)
	s_barrier
	s_waitcnt lgkmcnt(0)
	s_setprio 1
	v_mfma_scale_f32_16x16x128_f8f6f4 v[156:159], v[0:7], v[204:211], v[156:159], v188, v188 op_sel_hi:[0,0,0]
	v_mfma_scale_f32_16x16x128_f8f6f4 v[152:155], v[8:15], v[204:211], v[152:155], v188, v188 op_sel_hi:[0,0,0]
	v_mfma_scale_f32_16x16x128_f8f6f4 v[148:151], v[0:7], v[216:223], v[148:151], v188, v188 op_sel_hi:[0,0,0]
	v_mfma_scale_f32_16x16x128_f8f6f4 v[144:147], v[8:15], v[216:223], v[144:147], v188, v188 op_sel_hi:[0,0,0]
	v_mfma_scale_f32_16x16x128_f8f6f4 v[140:143], v[0:7], v[224:231], v[140:143], v188, v188 op_sel_hi:[0,0,0]
	v_mfma_scale_f32_16x16x128_f8f6f4 v[136:139], v[8:15], v[224:231], v[136:139], v188, v188 op_sel_hi:[0,0,0]
	v_mfma_scale_f32_16x16x128_f8f6f4 v[132:135], v[0:7], v[232:239], v[132:135], v188, v188 op_sel_hi:[0,0,0]
	v_mfma_scale_f32_16x16x128_f8f6f4 v[128:131], v[8:15], v[232:239], v[128:131], v188, v188 op_sel_hi:[0,0,0]
	s_setprio 0
	s_barrier
	s_mov_b32 m0, s15
	v_lshl_add_u64 v[180:181], s[24:25], 0, v[162:163]
	ds_read_b128 v[16:19], v190 offset:16384
	ds_read_b128 v[24:27], v190 offset:18432
	ds_read_b128 v[20:23], v192 offset:16384
	ds_read_b128 v[28:31], v192 offset:18432
	global_load_lds_dwordx4 v[180:181], off
	v_lshl_add_u64 v[182:183], s[24:25], 0, v[164:165]
	s_mov_b32 m0, s31
	s_nop 0
	global_load_lds_dwordx4 v[182:183], off
	s_barrier
	s_waitcnt lgkmcnt(0)
	s_setprio 1
	v_mfma_scale_f32_16x16x128_f8f6f4 v[100:103], v[16:23], v[204:211], v[100:103], v188, v188 op_sel_hi:[0,0,0]
	v_mfma_scale_f32_16x16x128_f8f6f4 v[96:99], v[24:31], v[204:211], v[96:99], v188, v188 op_sel_hi:[0,0,0]
	v_mfma_scale_f32_16x16x128_f8f6f4 v[84:87], v[16:23], v[216:223], v[84:87], v188, v188 op_sel_hi:[0,0,0]
	v_mfma_scale_f32_16x16x128_f8f6f4 v[80:83], v[24:31], v[216:223], v[80:83], v188, v188 op_sel_hi:[0,0,0]
	v_mfma_scale_f32_16x16x128_f8f6f4 v[76:79], v[16:23], v[224:231], v[76:79], v188, v188 op_sel_hi:[0,0,0]
	v_mfma_scale_f32_16x16x128_f8f6f4 v[72:75], v[24:31], v[224:231], v[72:75], v188, v188 op_sel_hi:[0,0,0]
	v_mfma_scale_f32_16x16x128_f8f6f4 v[68:71], v[16:23], v[232:239], v[68:71], v188, v188 op_sel_hi:[0,0,0]
	v_mfma_scale_f32_16x16x128_f8f6f4 v[64:67], v[24:31], v[232:239], v[64:67], v188, v188 op_sel_hi:[0,0,0]
	s_setprio 0
	s_mov_b32 m0, s13
	s_barrier
	ds_read_b128 v[204:207], v189 offset:16384
	ds_read_b128 v[216:219], v189 offset:18432
	ds_read_b128 v[208:211], v191 offset:16384
	ds_read_b128 v[220:223], v191 offset:18432
	ds_read_b128 v[224:227], v189 offset:20480
	ds_read_b128 v[232:235], v189 offset:22528
	ds_read_b128 v[228:231], v191 offset:20480
	ds_read_b128 v[236:239], v191 offset:22528
	global_load_lds_dwordx4 v172, s[26:27]
	s_mov_b32 m0, s44
	v_mov_b32_e32 v185, v173
	global_load_lds_dwordx4 v184, s[26:27]
	s_barrier
	s_waitcnt lgkmcnt(0)
	v_lshl_add_u64 v[186:187], s[26:27], 0, v[172:173]
	v_lshl_add_u64 v[184:185], s[26:27], 0, v[184:185]
	s_setprio 1
	s_waitcnt lgkmcnt(0)
	v_mfma_scale_f32_16x16x128_f8f6f4 v[124:127], v[0:7], v[204:211], v[124:127], v188, v188 op_sel_hi:[0,0,0]
	v_mfma_scale_f32_16x16x128_f8f6f4 v[120:123], v[8:15], v[204:211], v[120:123], v188, v188 op_sel_hi:[0,0,0]
	v_mfma_scale_f32_16x16x128_f8f6f4 v[116:119], v[0:7], v[216:223], v[116:119], v188, v188 op_sel_hi:[0,0,0]
	v_mfma_scale_f32_16x16x128_f8f6f4 v[112:115], v[8:15], v[216:223], v[112:115], v188, v188 op_sel_hi:[0,0,0]
	v_mfma_scale_f32_16x16x128_f8f6f4 v[108:111], v[0:7], v[224:231], v[108:111], v188, v188 op_sel_hi:[0,0,0]
	v_mfma_scale_f32_16x16x128_f8f6f4 v[104:107], v[8:15], v[224:231], v[104:107], v188, v188 op_sel_hi:[0,0,0]
	v_mfma_scale_f32_16x16x128_f8f6f4 v[92:95], v[0:7], v[232:239], v[92:95], v188, v188 op_sel_hi:[0,0,0]
	v_mfma_scale_f32_16x16x128_f8f6f4 v[88:91], v[8:15], v[232:239], v[88:91], v188, v188 op_sel_hi:[0,0,0]
	s_setprio 0
	s_barrier
	s_add_u32 s90, s24, 0x20000
	s_addc_u32 s91, s25, 0
	s_mov_b32 m0, s46
	v_lshl_add_u64 v[0:1], s[90:91], 0, v[162:163]
	global_load_lds_dwordx4 v[0:1], off
	v_lshl_add_u64 v[0:1], s[90:91], 0, v[164:165]
	s_mov_b32 m0, s47
	s_nop 0
	global_load_lds_dwordx4 v[0:1], off
	s_waitcnt vmcnt(6)
	s_barrier
	s_setprio 1
	v_mfma_scale_f32_16x16x128_f8f6f4 v[60:63], v[16:23], v[204:211], v[60:63], v188, v188 op_sel_hi:[0,0,0]
	v_mfma_scale_f32_16x16x128_f8f6f4 v[56:59], v[24:31], v[204:211], v[56:59], v188, v188 op_sel_hi:[0,0,0]
	v_mfma_scale_f32_16x16x128_f8f6f4 v[52:55], v[16:23], v[216:223], v[52:55], v188, v188 op_sel_hi:[0,0,0]
	v_mfma_scale_f32_16x16x128_f8f6f4 v[48:51], v[24:31], v[216:223], v[48:51], v188, v188 op_sel_hi:[0,0,0]
	v_mfma_scale_f32_16x16x128_f8f6f4 v[44:47], v[16:23], v[224:231], v[44:47], v188, v188 op_sel_hi:[0,0,0]
	v_mfma_scale_f32_16x16x128_f8f6f4 v[40:43], v[24:31], v[224:231], v[40:43], v188, v188 op_sel_hi:[0,0,0]
	v_mfma_scale_f32_16x16x128_f8f6f4 v[36:39], v[16:23], v[232:239], v[36:39], v188, v188 op_sel_hi:[0,0,0]
	v_mfma_scale_f32_16x16x128_f8f6f4 v[32:35], v[24:31], v[232:239], v[32:35], v188, v188 op_sel_hi:[0,0,0]
	s_setprio 0
	s_barrier
	ds_read_b128 v[0:3], v190 offset:32768
	ds_read_b128 v[8:11], v190 offset:34816
	ds_read_b128 v[4:7], v192 offset:32768
	ds_read_b128 v[12:15], v192 offset:34816
	s_mov_b32 m0, s50
	v_lshl_add_u64 v[178:179], s[26:27], 0, v[178:179]
	ds_read_b128 v[16:19], v189 offset:32768
	ds_read_b128 v[24:27], v189 offset:34816
	ds_read_b128 v[20:23], v191 offset:32768
	ds_read_b128 v[28:31], v191 offset:34816
	ds_read_b128 v[204:207], v189 offset:36864
	ds_read_b128 v[216:219], v189 offset:38912
	ds_read_b128 v[208:211], v191 offset:36864
	ds_read_b128 v[220:223], v191 offset:38912
	global_load_lds_dwordx4 v[178:179], off
	v_lshl_add_u64 v[176:177], s[26:27], 0, v[176:177]
	s_mov_b32 m0, s51
	s_nop 0
	global_load_lds_dwordx4 v[176:177], off
	s_waitcnt lgkmcnt(8)
	s_barrier
	s_waitcnt lgkmcnt(0)
	s_setprio 1
	v_mfma_scale_f32_16x16x128_f8f6f4 v[156:159], v[0:7], v[16:23], v[156:159], v188, v188 op_sel_hi:[0,0,0]
	v_mfma_scale_f32_16x16x128_f8f6f4 v[152:155], v[8:15], v[16:23], v[152:155], v188, v188 op_sel_hi:[0,0,0]
	v_mfma_scale_f32_16x16x128_f8f6f4 v[148:151], v[0:7], v[24:31], v[148:151], v188, v188 op_sel_hi:[0,0,0]
	v_mfma_scale_f32_16x16x128_f8f6f4 v[144:147], v[8:15], v[24:31], v[144:147], v188, v188 op_sel_hi:[0,0,0]
	v_mfma_scale_f32_16x16x128_f8f6f4 v[140:143], v[0:7], v[204:211], v[140:143], v188, v188 op_sel_hi:[0,0,0]
	v_mfma_scale_f32_16x16x128_f8f6f4 v[136:139], v[8:15], v[204:211], v[136:139], v188, v188 op_sel_hi:[0,0,0]
	v_mfma_scale_f32_16x16x128_f8f6f4 v[132:135], v[0:7], v[216:223], v[132:135], v188, v188 op_sel_hi:[0,0,0]
	v_mfma_scale_f32_16x16x128_f8f6f4 v[128:131], v[8:15], v[216:223], v[128:131], v188, v188 op_sel_hi:[0,0,0]
	s_setprio 0
	s_barrier
	s_mov_b32 m0, s56
	v_lshl_add_u64 v[176:177], v[180:181], 0, s[40:41]
	ds_read_b128 v[224:227], v190 offset:49152
	ds_read_b128 v[232:235], v190 offset:51200
	ds_read_b128 v[228:231], v192 offset:49152
	ds_read_b128 v[236:239], v192 offset:51200
	global_load_lds_dwordx4 v[176:177], off
	v_lshl_add_u64 v[176:177], v[182:183], 0, s[40:41]
	s_mov_b32 m0, s57
	s_nop 0
	global_load_lds_dwordx4 v[176:177], off
	s_barrier
	s_waitcnt lgkmcnt(0)
	s_setprio 1
	v_mfma_scale_f32_16x16x128_f8f6f4 v[100:103], v[224:231], v[16:23], v[100:103], v188, v188 op_sel_hi:[0,0,0]
	v_mfma_scale_f32_16x16x128_f8f6f4 v[96:99], v[232:239], v[16:23], v[96:99], v188, v188 op_sel_hi:[0,0,0]
	v_mfma_scale_f32_16x16x128_f8f6f4 v[84:87], v[224:231], v[24:31], v[84:87], v188, v188 op_sel_hi:[0,0,0]
	v_mfma_scale_f32_16x16x128_f8f6f4 v[80:83], v[232:239], v[24:31], v[80:83], v188, v188 op_sel_hi:[0,0,0]
	v_mfma_scale_f32_16x16x128_f8f6f4 v[76:79], v[224:231], v[204:211], v[76:79], v188, v188 op_sel_hi:[0,0,0]
	v_mfma_scale_f32_16x16x128_f8f6f4 v[72:75], v[232:239], v[204:211], v[72:75], v188, v188 op_sel_hi:[0,0,0]
	v_mfma_scale_f32_16x16x128_f8f6f4 v[68:71], v[224:231], v[216:223], v[68:71], v188, v188 op_sel_hi:[0,0,0]
	v_mfma_scale_f32_16x16x128_f8f6f4 v[64:67], v[232:239], v[216:223], v[64:67], v188, v188 op_sel_hi:[0,0,0]
	s_setprio 0
	s_mov_b32 m0, s64
	v_lshl_add_u64 v[186:187], v[186:187], 0, s[40:41]
	s_barrier
	ds_read_b128 v[16:19], v189 offset:49152
	ds_read_b128 v[24:27], v189 offset:51200
	ds_read_b128 v[20:23], v191 offset:49152
	ds_read_b128 v[28:31], v191 offset:51200
	ds_read_b128 v[176:179], v189 offset:53248
	ds_read_b128 v[204:207], v189 offset:55296
	ds_read_b128 v[180:183], v191 offset:53248
	ds_read_b128 v[208:211], v191 offset:55296
	global_load_lds_dwordx4 v[186:187], off
	v_lshl_add_u64 v[184:185], v[184:185], 0, s[40:41]
	s_mov_b32 m0, s65
	s_nop 0
	global_load_lds_dwordx4 v[184:185], off
	s_barrier
	s_waitcnt lgkmcnt(0)
	s_setprio 1
	v_mfma_scale_f32_16x16x128_f8f6f4 v[124:127], v[0:7], v[16:23], v[124:127], v188, v188 op_sel_hi:[0,0,0]
	v_mfma_scale_f32_16x16x128_f8f6f4 v[120:123], v[8:15], v[16:23], v[120:123], v188, v188 op_sel_hi:[0,0,0]
	v_mfma_scale_f32_16x16x128_f8f6f4 v[116:119], v[0:7], v[24:31], v[116:119], v188, v188 op_sel_hi:[0,0,0]
	v_mfma_scale_f32_16x16x128_f8f6f4 v[112:115], v[8:15], v[24:31], v[112:115], v188, v188 op_sel_hi:[0,0,0]
	v_mfma_scale_f32_16x16x128_f8f6f4 v[108:111], v[0:7], v[176:183], v[108:111], v188, v188 op_sel_hi:[0,0,0]
	v_mfma_scale_f32_16x16x128_f8f6f4 v[104:107], v[8:15], v[176:183], v[104:107], v188, v188 op_sel_hi:[0,0,0]
	v_mfma_scale_f32_16x16x128_f8f6f4 v[92:95], v[0:7], v[204:211], v[92:95], v188, v188 op_sel_hi:[0,0,0]
	v_mfma_scale_f32_16x16x128_f8f6f4 v[88:91], v[8:15], v[204:211], v[88:91], v188, v188 op_sel_hi:[0,0,0]
	s_setprio 0
	s_barrier
	s_add_u32 s24, s24, 0x20080
	s_addc_u32 s25, s25, 0
	s_mov_b32 m0, s70
	v_lshl_add_u64 v[0:1], s[24:25], 0, v[162:163]
	global_load_lds_dwordx4 v[0:1], off
	v_lshl_add_u64 v[0:1], s[24:25], 0, v[164:165]
	s_mov_b32 m0, s71
	s_nop 0
	global_load_lds_dwordx4 v[0:1], off
	s_waitcnt vmcnt(6)
	s_barrier
	s_setprio 1
	v_mfma_scale_f32_16x16x128_f8f6f4 v[60:63], v[224:231], v[16:23], v[60:63], v188, v188 op_sel_hi:[0,0,0]
	v_mfma_scale_f32_16x16x128_f8f6f4 v[56:59], v[232:239], v[16:23], v[56:59], v188, v188 op_sel_hi:[0,0,0]
	v_mfma_scale_f32_16x16x128_f8f6f4 v[52:55], v[224:231], v[24:31], v[52:55], v188, v188 op_sel_hi:[0,0,0]
	v_mfma_scale_f32_16x16x128_f8f6f4 v[48:51], v[232:239], v[24:31], v[48:51], v188, v188 op_sel_hi:[0,0,0]
	v_mfma_scale_f32_16x16x128_f8f6f4 v[44:47], v[224:231], v[176:183], v[44:47], v188, v188 op_sel_hi:[0,0,0]
	v_mfma_scale_f32_16x16x128_f8f6f4 v[40:43], v[232:239], v[176:183], v[40:43], v188, v188 op_sel_hi:[0,0,0]
	v_mfma_scale_f32_16x16x128_f8f6f4 v[36:39], v[224:231], v[204:211], v[36:39], v188, v188 op_sel_hi:[0,0,0]
	v_mfma_scale_f32_16x16x128_f8f6f4 v[32:35], v[232:239], v[204:211], v[32:35], v188, v188 op_sel_hi:[0,0,0]
	s_setprio 0
	s_add_i32 s85, s85, 2
	s_add_u32 s22, s22, 0x100
	s_addc_u32 s23, s23, 0
	s_add_u32 s7, s7, 0x100
	s_addc_u32 s83, s83, 0
	s_cmp_gt_u32 s85, 5
	s_barrier
	s_cbranch_scc1 .LBB0_1655
